# all s_setprio toggles around the GEMM MFMA blocks deleted (everything at priority 0), on top of the phase-11 reordering
# speedup vs baseline: 1.0225x; 1.0225x over previous
.LBB0_261:
	ds_read_b128 v[144:147], v170
	ds_read_b128 v[148:151], v170 offset:1024
	ds_read_b128 v[174:177], v170 offset:2048
	ds_read_b128 v[178:181], v170 offset:3072
	ds_read_b128 v[182:185], v171
	ds_read_b128 v[186:189], v171 offset:1024
	ds_read_b128 v[190:193], v171 offset:2048
	ds_read_b128 v[194:197], v171 offset:3072
	s_add_u32 s26, s80, 0xfff80080
	s_addc_u32 s27, s81, -1
	s_cmp_eq_u32 vcc_hi, 28
	s_cselect_b32 s83, s69, s27
	s_cselect_b32 s82, s75, s26
	s_cselect_b32 s27, s57, vcc_lo
	s_cselect_b32 s26, s96, s97
	v_lshl_add_u64 v[152:153], s[80:81], 0, v[134:135]
	s_add_i32 m0, s87, 0xc000
	ds_read_b128 v[198:201], v172
	ds_read_b128 v[202:205], v172 offset:1024
	ds_read_b128 v[206:209], v172 offset:2048
	ds_read_b128 v[210:213], v172 offset:3072
	ds_read_b128 v[214:217], v172 offset:4096
	ds_read_b128 v[220:223], v172 offset:5120
	ds_read_b128 v[224:227], v172 offset:6144
	ds_read_b128 v[228:231], v172 offset:7168
	global_load_lds_dwordx4 v[152:153], off
	v_lshl_add_u64 v[152:153], s[80:81], 0, v[138:139]
	s_add_i32 m0, s87, 0xe000
	s_nop 0
	global_load_lds_dwordx4 v[152:153], off
	s_waitcnt vmcnt(8)
	s_waitcnt lgkmcnt(0)
	s_barrier
	s_waitcnt lgkmcnt(0)
	v_mfma_f32_16x16x32_bf16 v[122:125], v[144:147], v[198:201], v[122:125]
	v_mfma_f32_16x16x32_bf16 v[118:121], v[174:177], v[198:201], v[118:121]
	v_mfma_f32_16x16x32_bf16 v[106:109], v[144:147], v[206:209], v[106:109]
	v_mfma_f32_16x16x32_bf16 v[102:105], v[174:177], v[206:209], v[102:105]
	v_mfma_f32_16x16x32_bf16 v[90:93], v[144:147], v[214:217], v[90:93]
	v_mfma_f32_16x16x32_bf16 v[86:89], v[174:177], v[214:217], v[86:89]
	v_mfma_f32_16x16x32_bf16 v[74:77], v[144:147], v[224:227], v[74:77]
	v_mfma_f32_16x16x32_bf16 v[70:73], v[174:177], v[224:227], v[70:73]
	v_mfma_f32_16x16x32_bf16 v[122:125], v[148:151], v[202:205], v[122:125]
	v_mfma_f32_16x16x32_bf16 v[118:121], v[178:181], v[202:205], v[118:121]
	v_mfma_f32_16x16x32_bf16 v[106:109], v[148:151], v[210:213], v[106:109]
	v_mfma_f32_16x16x32_bf16 v[102:105], v[178:181], v[210:213], v[102:105]
	v_mfma_f32_16x16x32_bf16 v[90:93], v[148:151], v[220:223], v[90:93]
	v_mfma_f32_16x16x32_bf16 v[86:89], v[178:181], v[220:223], v[86:89]
	v_mfma_f32_16x16x32_bf16 v[74:77], v[148:151], v[228:231], v[74:77]
	v_mfma_f32_16x16x32_bf16 v[70:73], v[178:181], v[228:231], v[70:73]
	v_mfma_f32_16x16x32_bf16 v[126:129], v[182:185], v[198:201], v[126:129]
	v_mfma_f32_16x16x32_bf16 v[114:117], v[190:193], v[198:201], v[114:117]
	v_mfma_f32_16x16x32_bf16 v[110:113], v[182:185], v[206:209], v[110:113]
	v_mfma_f32_16x16x32_bf16 v[98:101], v[190:193], v[206:209], v[98:101]
	v_mfma_f32_16x16x32_bf16 v[94:97], v[182:185], v[214:217], v[94:97]
	v_mfma_f32_16x16x32_bf16 v[82:85], v[190:193], v[214:217], v[82:85]
	v_mfma_f32_16x16x32_bf16 v[78:81], v[182:185], v[224:227], v[78:81]
	v_mfma_f32_16x16x32_bf16 v[66:69], v[190:193], v[224:227], v[66:69]
	v_mfma_f32_16x16x32_bf16 v[126:129], v[186:189], v[202:205], v[126:129]
	v_mfma_f32_16x16x32_bf16 v[114:117], v[194:197], v[202:205], v[114:117]
	v_mfma_f32_16x16x32_bf16 v[110:113], v[186:189], v[210:213], v[110:113]
	v_mfma_f32_16x16x32_bf16 v[98:101], v[194:197], v[210:213], v[98:101]
	v_mfma_f32_16x16x32_bf16 v[94:97], v[186:189], v[220:223], v[94:97]
	v_mfma_f32_16x16x32_bf16 v[82:85], v[194:197], v[220:223], v[82:85]
	v_mfma_f32_16x16x32_bf16 v[78:81], v[186:189], v[228:231], v[78:81]
	v_mfma_f32_16x16x32_bf16 v[66:69], v[194:197], v[228:231], v[66:69]
	s_barrier
	v_lshl_add_u64 v[152:153], s[26:27], 0, v[162:163]
	s_add_i32 s26, s94, s86
	s_mov_b32 m0, s26
	ds_read_b128 v[198:201], v172 offset:16384
	ds_read_b128 v[202:205], v172 offset:17408
	ds_read_b128 v[206:209], v172 offset:18432
	ds_read_b128 v[210:213], v172 offset:19456
	ds_read_b128 v[214:217], v172 offset:20480
	ds_read_b128 v[220:223], v172 offset:21504
	ds_read_b128 v[224:227], v172 offset:22528
	ds_read_b128 v[228:231], v172 offset:23552
	global_load_lds_dwordx4 v[152:153], off
	v_lshl_add_u64 v[232:233], v[152:153], 0, s[10:11]
	s_add_i32 m0, s26, 0x2000
	s_add_i32 s26, s95, s86
	global_load_lds_dwordx4 v[232:233], off
	v_lshl_add_u64 v[232:233], v[152:153], 0, s[12:13]
	s_mov_b32 m0, s26
	v_lshl_add_u64 v[234:235], s[82:83], 0, v[132:133]
	global_load_lds_dwordx4 v[232:233], off
	v_lshl_add_u64 v[232:233], v[152:153], 0, s[14:15]
	s_add_i32 m0, s26, 0x2000
	s_nop 0
	global_load_lds_dwordx4 v[232:233], off
	v_lshl_add_u64 v[232:233], s[82:83], 0, v[130:131]
	s_mov_b32 m0, s87
	s_nop 0
	global_load_lds_dwordx4 v[232:233], off
	s_mov_b32 m0, s88
	s_nop 0
	global_load_lds_dwordx4 v[234:235], off
	s_waitcnt vmcnt(8)
	s_waitcnt lgkmcnt(0)
	s_barrier
	s_waitcnt lgkmcnt(0)
	v_mfma_f32_16x16x32_bf16 v[58:61], v[144:147], v[198:201], v[58:61]
	v_mfma_f32_16x16x32_bf16 v[54:57], v[174:177], v[198:201], v[54:57]
	v_mfma_f32_16x16x32_bf16 v[42:45], v[144:147], v[206:209], v[42:45]
	v_mfma_f32_16x16x32_bf16 v[38:41], v[174:177], v[206:209], v[38:41]
	v_mfma_f32_16x16x32_bf16 v[26:29], v[144:147], v[214:217], v[26:29]
	v_mfma_f32_16x16x32_bf16 v[22:25], v[174:177], v[214:217], v[22:25]
	v_mfma_f32_16x16x32_bf16 v[10:13], v[144:147], v[224:227], v[10:13]
	v_mfma_f32_16x16x32_bf16 v[6:9], v[174:177], v[224:227], v[6:9]
	v_mfma_f32_16x16x32_bf16 v[58:61], v[148:151], v[202:205], v[58:61]
	v_mfma_f32_16x16x32_bf16 v[54:57], v[178:181], v[202:205], v[54:57]
	v_mfma_f32_16x16x32_bf16 v[42:45], v[148:151], v[210:213], v[42:45]
	v_mfma_f32_16x16x32_bf16 v[38:41], v[178:181], v[210:213], v[38:41]
	v_mfma_f32_16x16x32_bf16 v[26:29], v[148:151], v[220:223], v[26:29]
	v_mfma_f32_16x16x32_bf16 v[22:25], v[178:181], v[220:223], v[22:25]
	v_mfma_f32_16x16x32_bf16 v[10:13], v[148:151], v[228:231], v[10:13]
	v_mfma_f32_16x16x32_bf16 v[6:9], v[178:181], v[228:231], v[6:9]
	v_mfma_f32_16x16x32_bf16 v[62:65], v[182:185], v[198:201], v[62:65]
	v_mfma_f32_16x16x32_bf16 v[50:53], v[190:193], v[198:201], v[50:53]
	v_mfma_f32_16x16x32_bf16 v[46:49], v[182:185], v[206:209], v[46:49]
	v_mfma_f32_16x16x32_bf16 v[34:37], v[190:193], v[206:209], v[34:37]
	v_mfma_f32_16x16x32_bf16 v[30:33], v[182:185], v[214:217], v[30:33]
	v_mfma_f32_16x16x32_bf16 v[18:21], v[190:193], v[214:217], v[18:21]
	v_mfma_f32_16x16x32_bf16 v[14:17], v[182:185], v[224:227], v[14:17]
	v_mfma_f32_16x16x32_bf16 v[2:5], v[190:193], v[224:227], v[2:5]
	v_mfma_f32_16x16x32_bf16 v[62:65], v[186:189], v[202:205], v[62:65]
	v_mfma_f32_16x16x32_bf16 v[50:53], v[194:197], v[202:205], v[50:53]
	v_mfma_f32_16x16x32_bf16 v[46:49], v[186:189], v[210:213], v[46:49]
	v_mfma_f32_16x16x32_bf16 v[34:37], v[194:197], v[210:213], v[34:37]
	v_mfma_f32_16x16x32_bf16 v[30:33], v[186:189], v[220:223], v[30:33]
	v_mfma_f32_16x16x32_bf16 v[18:21], v[194:197], v[220:223], v[18:21]
	v_mfma_f32_16x16x32_bf16 v[14:17], v[186:189], v[228:231], v[14:17]
	v_mfma_f32_16x16x32_bf16 v[2:5], v[194:197], v[228:231], v[2:5]
	s_barrier
	s_add_i32 s33, 0, 0x18000
	v_add_u32_e32 v136, s33, v167
	s_add_i32 s8, 0, 0x1c000
	ds_read_b128 v[144:147], v136
	ds_read_b128 v[148:151], v136 offset:1024
	ds_read_b128 v[174:177], v136 offset:2048
	ds_read_b128 v[178:181], v136 offset:3072
	v_add_u32_e32 v136, s8, v167
	ds_read_b128 v[182:185], v136
	ds_read_b128 v[186:189], v136 offset:1024
	ds_read_b128 v[190:193], v136 offset:2048
	ds_read_b128 v[194:197], v136 offset:3072
	s_add_u32 s26, s82, 0x80000
	s_addc_u32 s27, s83, 0
	s_mov_b32 m0, s89
	v_lshl_add_u64 v[236:237], s[26:27], 0, v[130:131]
	ds_read_b128 v[198:201], v172 offset:32768
	ds_read_b128 v[202:205], v172 offset:33792
	ds_read_b128 v[206:209], v172 offset:34816
	ds_read_b128 v[210:213], v172 offset:35840
	ds_read_b128 v[214:217], v172 offset:36864
	ds_read_b128 v[220:223], v172 offset:37888
	ds_read_b128 v[224:227], v172 offset:38912
	ds_read_b128 v[228:231], v172 offset:39936
	global_load_lds_dwordx4 v[236:237], off
	v_lshl_add_u64 v[236:237], s[26:27], 0, v[132:133]
	s_mov_b32 m0, s90
	s_nop 0
	global_load_lds_dwordx4 v[236:237], off
	s_waitcnt vmcnt(8)
	s_waitcnt lgkmcnt(0)
	s_barrier
	s_waitcnt lgkmcnt(0)
	v_mfma_f32_16x16x32_bf16 v[122:125], v[144:147], v[198:201], v[122:125]
	v_mfma_f32_16x16x32_bf16 v[118:121], v[174:177], v[198:201], v[118:121]
	v_mfma_f32_16x16x32_bf16 v[106:109], v[144:147], v[206:209], v[106:109]
	v_mfma_f32_16x16x32_bf16 v[102:105], v[174:177], v[206:209], v[102:105]
	v_mfma_f32_16x16x32_bf16 v[90:93], v[144:147], v[214:217], v[90:93]
	v_mfma_f32_16x16x32_bf16 v[86:89], v[174:177], v[214:217], v[86:89]
	v_mfma_f32_16x16x32_bf16 v[74:77], v[144:147], v[224:227], v[74:77]
	v_mfma_f32_16x16x32_bf16 v[70:73], v[174:177], v[224:227], v[70:73]
	v_mfma_f32_16x16x32_bf16 v[122:125], v[148:151], v[202:205], v[122:125]
	v_mfma_f32_16x16x32_bf16 v[118:121], v[178:181], v[202:205], v[118:121]
	v_mfma_f32_16x16x32_bf16 v[106:109], v[148:151], v[210:213], v[106:109]
	v_mfma_f32_16x16x32_bf16 v[102:105], v[178:181], v[210:213], v[102:105]
	v_mfma_f32_16x16x32_bf16 v[90:93], v[148:151], v[220:223], v[90:93]
	v_mfma_f32_16x16x32_bf16 v[86:89], v[178:181], v[220:223], v[86:89]
	v_mfma_f32_16x16x32_bf16 v[74:77], v[148:151], v[228:231], v[74:77]
	v_mfma_f32_16x16x32_bf16 v[70:73], v[178:181], v[228:231], v[70:73]
	v_mfma_f32_16x16x32_bf16 v[126:129], v[182:185], v[198:201], v[126:129]
	v_mfma_f32_16x16x32_bf16 v[114:117], v[190:193], v[198:201], v[114:117]
	v_mfma_f32_16x16x32_bf16 v[110:113], v[182:185], v[206:209], v[110:113]
	v_mfma_f32_16x16x32_bf16 v[98:101], v[190:193], v[206:209], v[98:101]
	v_mfma_f32_16x16x32_bf16 v[94:97], v[182:185], v[214:217], v[94:97]
	v_mfma_f32_16x16x32_bf16 v[82:85], v[190:193], v[214:217], v[82:85]
	v_mfma_f32_16x16x32_bf16 v[78:81], v[182:185], v[224:227], v[78:81]
	v_mfma_f32_16x16x32_bf16 v[66:69], v[190:193], v[224:227], v[66:69]
	v_mfma_f32_16x16x32_bf16 v[126:129], v[186:189], v[202:205], v[126:129]
	v_mfma_f32_16x16x32_bf16 v[114:117], v[194:197], v[202:205], v[114:117]
	v_mfma_f32_16x16x32_bf16 v[110:113], v[186:189], v[210:213], v[110:113]
	v_mfma_f32_16x16x32_bf16 v[98:101], v[194:197], v[210:213], v[98:101]
	v_mfma_f32_16x16x32_bf16 v[94:97], v[186:189], v[220:223], v[94:97]
	v_mfma_f32_16x16x32_bf16 v[82:85], v[194:197], v[220:223], v[82:85]
	v_mfma_f32_16x16x32_bf16 v[78:81], v[186:189], v[228:231], v[78:81]
	v_mfma_f32_16x16x32_bf16 v[66:69], v[194:197], v[228:231], v[66:69]
	s_barrier
	s_add_i32 s9, s33, s86
	v_lshl_add_u64 v[236:237], v[152:153], 0, s[20:21]
	s_mov_b32 m0, s9
	ds_read_b128 v[198:201], v172 offset:49152
	ds_read_b128 v[202:205], v172 offset:50176
	ds_read_b128 v[206:209], v172 offset:51200
	ds_read_b128 v[210:213], v172 offset:52224
	ds_read_b128 v[214:217], v172 offset:53248
	ds_read_b128 v[220:223], v172 offset:54272
	ds_read_b128 v[224:227], v172 offset:55296
	ds_read_b128 v[228:231], v172 offset:56320
	global_load_lds_dwordx4 v[236:237], off
	v_lshl_add_u64 v[236:237], v[152:153], 0, s[22:23]
	s_add_i32 m0, s9, 0x2000
	s_add_i32 s8, s8, s86
	global_load_lds_dwordx4 v[236:237], off
	v_lshl_add_u64 v[236:237], v[152:153], 0, s[40:41]
	s_mov_b32 m0, s8
	v_lshl_add_u64 v[152:153], v[152:153], 0, s[44:45]
	global_load_lds_dwordx4 v[236:237], off
	s_add_i32 m0, s8, 0x2000
	s_nop 0
	global_load_lds_dwordx4 v[152:153], off
	v_lshl_add_u64 v[152:153], v[232:233], 0, s[24:25]
	s_mov_b32 m0, s91
	s_nop 0
	global_load_lds_dwordx4 v[152:153], off
	v_lshl_add_u64 v[152:153], v[234:235], 0, s[24:25]
	s_mov_b32 m0, s92
	s_nop 0
	global_load_lds_dwordx4 v[152:153], off
	s_waitcnt vmcnt(8)
	s_waitcnt lgkmcnt(0)
	s_barrier
	s_waitcnt lgkmcnt(0)
	v_mfma_f32_16x16x32_bf16 v[58:61], v[144:147], v[198:201], v[58:61]
	v_mfma_f32_16x16x32_bf16 v[54:57], v[174:177], v[198:201], v[54:57]
	v_mfma_f32_16x16x32_bf16 v[42:45], v[144:147], v[206:209], v[42:45]
	v_mfma_f32_16x16x32_bf16 v[38:41], v[174:177], v[206:209], v[38:41]
	v_mfma_f32_16x16x32_bf16 v[26:29], v[144:147], v[214:217], v[26:29]
	v_mfma_f32_16x16x32_bf16 v[22:25], v[174:177], v[214:217], v[22:25]
	v_mfma_f32_16x16x32_bf16 v[10:13], v[144:147], v[224:227], v[10:13]
	v_mfma_f32_16x16x32_bf16 v[6:9], v[174:177], v[224:227], v[6:9]
	v_mfma_f32_16x16x32_bf16 v[58:61], v[148:151], v[202:205], v[58:61]
	v_mfma_f32_16x16x32_bf16 v[54:57], v[178:181], v[202:205], v[54:57]
	v_mfma_f32_16x16x32_bf16 v[42:45], v[148:151], v[210:213], v[42:45]
	v_mfma_f32_16x16x32_bf16 v[38:41], v[178:181], v[210:213], v[38:41]
	v_mfma_f32_16x16x32_bf16 v[26:29], v[148:151], v[220:223], v[26:29]
	v_mfma_f32_16x16x32_bf16 v[22:25], v[178:181], v[220:223], v[22:25]
	v_mfma_f32_16x16x32_bf16 v[10:13], v[148:151], v[228:231], v[10:13]
	v_mfma_f32_16x16x32_bf16 v[6:9], v[178:181], v[228:231], v[6:9]
	v_mfma_f32_16x16x32_bf16 v[62:65], v[182:185], v[198:201], v[62:65]
	v_mfma_f32_16x16x32_bf16 v[50:53], v[190:193], v[198:201], v[50:53]
	v_mfma_f32_16x16x32_bf16 v[46:49], v[182:185], v[206:209], v[46:49]
	v_mfma_f32_16x16x32_bf16 v[34:37], v[190:193], v[206:209], v[34:37]
	v_mfma_f32_16x16x32_bf16 v[30:33], v[182:185], v[214:217], v[30:33]
	v_mfma_f32_16x16x32_bf16 v[18:21], v[190:193], v[214:217], v[18:21]
	v_mfma_f32_16x16x32_bf16 v[14:17], v[182:185], v[224:227], v[14:17]
	v_mfma_f32_16x16x32_bf16 v[2:5], v[190:193], v[224:227], v[2:5]
	v_mfma_f32_16x16x32_bf16 v[62:65], v[186:189], v[202:205], v[62:65]
	v_mfma_f32_16x16x32_bf16 v[50:53], v[194:197], v[202:205], v[50:53]
	v_mfma_f32_16x16x32_bf16 v[46:49], v[186:189], v[210:213], v[46:49]
	v_mfma_f32_16x16x32_bf16 v[34:37], v[194:197], v[210:213], v[34:37]
	v_mfma_f32_16x16x32_bf16 v[30:33], v[186:189], v[220:223], v[30:33]
	v_mfma_f32_16x16x32_bf16 v[18:21], v[194:197], v[220:223], v[18:21]
	v_mfma_f32_16x16x32_bf16 v[14:17], v[186:189], v[228:231], v[14:17]
	v_mfma_f32_16x16x32_bf16 v[2:5], v[194:197], v[228:231], v[2:5]
	s_barrier
	s_add_i32 vcc_hi, vcc_hi, 2
	s_add_u32 s97, s97, 0x10000
	s_addc_u32 vcc_lo, vcc_lo, 0
	s_add_u32 s80, s80, 0x100
	s_addc_u32 s81, s81, 0
	s_cmp_gt_u32 vcc_hi, 29
	s_cbranch_scc0 .LBB0_261
	s_and_b64 vcc, exec, s[50:51]
	s_cbranch_vccz .LBB0_264
	s_barrier

.LBB0_285:
	ds_read_b128 v[26:29], v1
	ds_read_b128 v[30:33], v1 offset:1024
	ds_read_b128 v[18:21], v1 offset:2048
	ds_read_b128 v[22:25], v1 offset:3072
	ds_read_b128 v[10:13], v185
	ds_read_b128 v[14:17], v185 offset:1024
	ds_read_b128 v[2:5], v185 offset:2048
	ds_read_b128 v[6:9], v185 offset:3072
	s_add_u32 s26, s70, 0xfffc0080
	s_addc_u32 s27, s71, -1
	s_cmp_eq_u32 s94, 12
	s_cselect_b32 s73, s51, s27
	s_cselect_b32 s72, s90, s26
	s_cselect_b32 s75, s45, s93
	s_cselect_b32 s74, s91, s92
	v_lshl_add_u64 v[176:177], s[70:71], 0, v[168:169]
	s_add_i32 m0, s33, 0xc000
	ds_read_b128 v[190:193], v186
	ds_read_b128 v[194:197], v186 offset:1024
	ds_read_b128 v[198:201], v186 offset:2048
	ds_read_b128 v[202:205], v186 offset:3072
	ds_read_b128 v[206:209], v186 offset:4096
	ds_read_b128 v[210:213], v186 offset:5120
	ds_read_b128 v[220:223], v186 offset:6144
	ds_read_b128 v[224:227], v186 offset:7168
	global_load_lds_dwordx4 v[176:177], off
	v_lshl_add_u64 v[176:177], s[70:71], 0, v[170:171]
	s_add_i32 m0, s33, 0xe000
	s_nop 0
	global_load_lds_dwordx4 v[176:177], off
	s_waitcnt vmcnt(8)
	s_waitcnt lgkmcnt(0)
	s_barrier
	s_waitcnt lgkmcnt(0)
	v_mfma_scale_f32_16x16x128_f8f6f4 v[158:161], v[26:33], v[190:197], v[158:161], v187, v188 op_sel_hi:[0,0,0]
	v_mfma_scale_f32_16x16x128_f8f6f4 v[154:157], v[18:25], v[190:197], v[154:157], v187, v188 op_sel_hi:[0,0,0]
	v_mfma_scale_f32_16x16x128_f8f6f4 v[150:153], v[26:33], v[198:205], v[150:153], v187, v188 op_sel_hi:[0,0,0]
	v_mfma_scale_f32_16x16x128_f8f6f4 v[142:145], v[18:25], v[198:205], v[142:145], v187, v188 op_sel_hi:[0,0,0]
	v_mfma_scale_f32_16x16x128_f8f6f4 v[134:137], v[26:33], v[206:213], v[134:137], v187, v188 op_sel_hi:[0,0,0]
	v_mfma_scale_f32_16x16x128_f8f6f4 v[126:129], v[18:25], v[206:213], v[126:129], v187, v188 op_sel_hi:[0,0,0]
	v_mfma_scale_f32_16x16x128_f8f6f4 v[118:121], v[26:33], v[220:227], v[118:121], v187, v188 op_sel_hi:[0,0,0]
	v_mfma_scale_f32_16x16x128_f8f6f4 v[110:113], v[18:25], v[220:227], v[110:113], v187, v188 op_sel_hi:[0,0,0]
	v_mfma_scale_f32_16x16x128_f8f6f4 v[146:149], v[10:17], v[190:197], v[146:149], v187, v188 op_sel_hi:[0,0,0]
	v_mfma_scale_f32_16x16x128_f8f6f4 v[138:141], v[2:9], v[190:197], v[138:141], v187, v188 op_sel_hi:[0,0,0]
	v_mfma_scale_f32_16x16x128_f8f6f4 v[130:133], v[10:17], v[198:205], v[130:133], v187, v188 op_sel_hi:[0,0,0]
	v_mfma_scale_f32_16x16x128_f8f6f4 v[122:125], v[2:9], v[198:205], v[122:125], v187, v188 op_sel_hi:[0,0,0]
	v_mfma_scale_f32_16x16x128_f8f6f4 v[114:117], v[10:17], v[206:213], v[114:117], v187, v188 op_sel_hi:[0,0,0]
	v_mfma_scale_f32_16x16x128_f8f6f4 v[106:109], v[2:9], v[206:213], v[106:109], v187, v188 op_sel_hi:[0,0,0]
	v_mfma_scale_f32_16x16x128_f8f6f4 v[102:105], v[10:17], v[220:227], v[102:105], v187, v188 op_sel_hi:[0,0,0]
	v_mfma_scale_f32_16x16x128_f8f6f4 v[98:101], v[2:9], v[220:227], v[98:101], v187, v188 op_sel_hi:[0,0,0]
	s_barrier
	s_add_i32 s26, s88, s80
	v_lshl_add_u64 v[176:177], s[74:75], 0, v[162:163]
	s_mov_b32 m0, s26
	ds_read_b128 v[190:193], v186 offset:16384
	ds_read_b128 v[194:197], v186 offset:17408
	ds_read_b128 v[198:201], v186 offset:18432
	ds_read_b128 v[202:205], v186 offset:19456
	ds_read_b128 v[206:209], v186 offset:20480
	ds_read_b128 v[210:213], v186 offset:21504
	ds_read_b128 v[220:223], v186 offset:22528
	ds_read_b128 v[224:227], v186 offset:23552
	global_load_lds_dwordx4 v[176:177], off
	v_lshl_add_u64 v[178:179], v[176:177], 0, s[8:9]
	s_add_i32 m0, s26, 0x2000
	s_add_i32 s26, s89, s80
	global_load_lds_dwordx4 v[178:179], off
	v_lshl_add_u64 v[178:179], v[176:177], 0, s[10:11]
	s_mov_b32 m0, s26
	v_lshl_add_u64 v[180:181], s[72:73], 0, v[166:167]
	global_load_lds_dwordx4 v[178:179], off
	v_lshl_add_u64 v[178:179], v[176:177], 0, s[12:13]
	s_add_i32 m0, s26, 0x2000
	s_nop 0
	global_load_lds_dwordx4 v[178:179], off
	v_lshl_add_u64 v[178:179], s[72:73], 0, v[164:165]
	s_mov_b32 m0, s33
	s_nop 0
	global_load_lds_dwordx4 v[178:179], off
	s_mov_b32 m0, s69
	s_nop 0
	global_load_lds_dwordx4 v[180:181], off
	s_waitcnt vmcnt(8)
	s_waitcnt lgkmcnt(0)
	s_barrier
	s_waitcnt lgkmcnt(0)
	v_mfma_scale_f32_16x16x128_f8f6f4 v[94:97], v[26:33], v[190:197], v[94:97], v187, v188 op_sel_hi:[0,0,0]
	v_mfma_scale_f32_16x16x128_f8f6f4 v[90:93], v[18:25], v[190:197], v[90:93], v187, v188 op_sel_hi:[0,0,0]
	v_mfma_scale_f32_16x16x128_f8f6f4 v[86:89], v[26:33], v[198:205], v[86:89], v187, v188 op_sel_hi:[0,0,0]
	v_mfma_scale_f32_16x16x128_f8f6f4 v[78:81], v[18:25], v[198:205], v[78:81], v187, v188 op_sel_hi:[0,0,0]
	v_mfma_scale_f32_16x16x128_f8f6f4 v[70:73], v[26:33], v[206:213], v[70:73], v187, v188 op_sel_hi:[0,0,0]
	v_mfma_scale_f32_16x16x128_f8f6f4 v[62:65], v[18:25], v[206:213], v[62:65], v187, v188 op_sel_hi:[0,0,0]
	v_mfma_scale_f32_16x16x128_f8f6f4 v[54:57], v[26:33], v[220:227], v[54:57], v187, v188 op_sel_hi:[0,0,0]
	v_mfma_scale_f32_16x16x128_f8f6f4 v[46:49], v[18:25], v[220:227], v[46:49], v187, v188 op_sel_hi:[0,0,0]
	v_mfma_scale_f32_16x16x128_f8f6f4 v[82:85], v[10:17], v[190:197], v[82:85], v187, v188 op_sel_hi:[0,0,0]
	v_mfma_scale_f32_16x16x128_f8f6f4 v[74:77], v[2:9], v[190:197], v[74:77], v187, v188 op_sel_hi:[0,0,0]
	v_mfma_scale_f32_16x16x128_f8f6f4 v[66:69], v[10:17], v[198:205], v[66:69], v187, v188 op_sel_hi:[0,0,0]
	v_mfma_scale_f32_16x16x128_f8f6f4 v[58:61], v[2:9], v[198:205], v[58:61], v187, v188 op_sel_hi:[0,0,0]
	v_mfma_scale_f32_16x16x128_f8f6f4 v[50:53], v[10:17], v[206:213], v[50:53], v187, v188 op_sel_hi:[0,0,0]
	v_mfma_scale_f32_16x16x128_f8f6f4 v[42:45], v[2:9], v[206:213], v[42:45], v187, v188 op_sel_hi:[0,0,0]
	v_mfma_scale_f32_16x16x128_f8f6f4 v[38:41], v[10:17], v[220:227], v[38:41], v187, v188 op_sel_hi:[0,0,0]
	v_mfma_scale_f32_16x16x128_f8f6f4 v[34:37], v[2:9], v[220:227], v[34:37], v187, v188 op_sel_hi:[0,0,0]
	s_barrier
	s_add_i32 s74, 0, 0x18000
	s_add_i32 s75, 0, 0x1c000
	v_add_u32_e32 v14, s74, v183
	v_add_u32_e32 v30, s75, v183
	ds_read_b128 v[2:5], v14
	ds_read_b128 v[6:9], v14 offset:1024
	ds_read_b128 v[10:13], v14 offset:2048
	ds_read_b128 v[14:17], v14 offset:3072
	ds_read_b128 v[18:21], v30
	ds_read_b128 v[22:25], v30 offset:1024
	ds_read_b128 v[26:29], v30 offset:2048
	ds_read_b128 v[30:33], v30 offset:3072
	s_add_u32 s26, s72, 0x40000
	s_addc_u32 s27, s73, 0
	s_mov_b32 m0, s83
	v_lshl_add_u64 v[214:215], s[26:27], 0, v[164:165]
	ds_read_b128 v[190:193], v186 offset:32768
	ds_read_b128 v[194:197], v186 offset:33792
	ds_read_b128 v[198:201], v186 offset:34816
	ds_read_b128 v[202:205], v186 offset:35840
	ds_read_b128 v[206:209], v186 offset:36864
	ds_read_b128 v[210:213], v186 offset:37888
	ds_read_b128 v[220:223], v186 offset:38912
	ds_read_b128 v[224:227], v186 offset:39936
	global_load_lds_dwordx4 v[214:215], off
	v_lshl_add_u64 v[214:215], s[26:27], 0, v[166:167]
	s_mov_b32 m0, s84
	s_nop 0
	global_load_lds_dwordx4 v[214:215], off
	s_waitcnt vmcnt(8)
	s_waitcnt lgkmcnt(0)
	s_barrier
	s_waitcnt lgkmcnt(0)
	v_mfma_scale_f32_16x16x128_f8f6f4 v[158:161], v[2:9], v[190:197], v[158:161], v187, v188 op_sel_hi:[0,0,0]
	v_mfma_scale_f32_16x16x128_f8f6f4 v[154:157], v[10:17], v[190:197], v[154:157], v187, v188 op_sel_hi:[0,0,0]
	v_mfma_scale_f32_16x16x128_f8f6f4 v[150:153], v[2:9], v[198:205], v[150:153], v187, v188 op_sel_hi:[0,0,0]
	v_mfma_scale_f32_16x16x128_f8f6f4 v[142:145], v[10:17], v[198:205], v[142:145], v187, v188 op_sel_hi:[0,0,0]
	v_mfma_scale_f32_16x16x128_f8f6f4 v[134:137], v[2:9], v[206:213], v[134:137], v187, v188 op_sel_hi:[0,0,0]
	v_mfma_scale_f32_16x16x128_f8f6f4 v[126:129], v[10:17], v[206:213], v[126:129], v187, v188 op_sel_hi:[0,0,0]
	v_mfma_scale_f32_16x16x128_f8f6f4 v[118:121], v[2:9], v[220:227], v[118:121], v187, v188 op_sel_hi:[0,0,0]
	v_mfma_scale_f32_16x16x128_f8f6f4 v[110:113], v[10:17], v[220:227], v[110:113], v187, v188 op_sel_hi:[0,0,0]
	v_mfma_scale_f32_16x16x128_f8f6f4 v[146:149], v[18:25], v[190:197], v[146:149], v187, v188 op_sel_hi:[0,0,0]
	v_mfma_scale_f32_16x16x128_f8f6f4 v[138:141], v[26:33], v[190:197], v[138:141], v187, v188 op_sel_hi:[0,0,0]
	v_mfma_scale_f32_16x16x128_f8f6f4 v[130:133], v[18:25], v[198:205], v[130:133], v187, v188 op_sel_hi:[0,0,0]
	v_mfma_scale_f32_16x16x128_f8f6f4 v[122:125], v[26:33], v[198:205], v[122:125], v187, v188 op_sel_hi:[0,0,0]
	v_mfma_scale_f32_16x16x128_f8f6f4 v[114:117], v[18:25], v[206:213], v[114:117], v187, v188 op_sel_hi:[0,0,0]
	v_mfma_scale_f32_16x16x128_f8f6f4 v[106:109], v[26:33], v[206:213], v[106:109], v187, v188 op_sel_hi:[0,0,0]
	v_mfma_scale_f32_16x16x128_f8f6f4 v[102:105], v[18:25], v[220:227], v[102:105], v187, v188 op_sel_hi:[0,0,0]
	v_mfma_scale_f32_16x16x128_f8f6f4 v[98:101], v[26:33], v[220:227], v[98:101], v187, v188 op_sel_hi:[0,0,0]
	s_barrier
	s_add_i32 s26, s74, s80
	v_lshl_add_u64 v[214:215], v[176:177], 0, s[16:17]
	s_mov_b32 m0, s26
	ds_read_b128 v[190:193], v186 offset:49152
	ds_read_b128 v[194:197], v186 offset:50176
	ds_read_b128 v[198:201], v186 offset:51200
	ds_read_b128 v[202:205], v186 offset:52224
	ds_read_b128 v[206:209], v186 offset:53248
	ds_read_b128 v[210:213], v186 offset:54272
	ds_read_b128 v[220:223], v186 offset:55296
	ds_read_b128 v[224:227], v186 offset:56320
	global_load_lds_dwordx4 v[214:215], off
	v_lshl_add_u64 v[214:215], v[176:177], 0, s[18:19]
	s_add_i32 m0, s26, 0x2000
	s_add_i32 s26, s75, s80
	global_load_lds_dwordx4 v[214:215], off
	v_lshl_add_u64 v[214:215], v[176:177], 0, s[22:23]
	s_mov_b32 m0, s26
	v_lshl_add_u64 v[176:177], v[176:177], 0, s[24:25]
	global_load_lds_dwordx4 v[214:215], off
	s_add_i32 m0, s26, 0x2000
	s_nop 0
	global_load_lds_dwordx4 v[176:177], off
	v_lshl_add_u64 v[176:177], v[178:179], 0, s[20:21]
	s_mov_b32 m0, s86
	s_nop 0
	global_load_lds_dwordx4 v[176:177], off
	v_lshl_add_u64 v[176:177], v[180:181], 0, s[20:21]
	s_mov_b32 m0, s87
	s_nop 0
	global_load_lds_dwordx4 v[176:177], off
	s_waitcnt vmcnt(8)
	s_waitcnt lgkmcnt(0)
	s_barrier
	s_waitcnt lgkmcnt(0)
	v_mfma_scale_f32_16x16x128_f8f6f4 v[94:97], v[2:9], v[190:197], v[94:97], v187, v188 op_sel_hi:[0,0,0]
	v_mfma_scale_f32_16x16x128_f8f6f4 v[90:93], v[10:17], v[190:197], v[90:93], v187, v188 op_sel_hi:[0,0,0]
	v_mfma_scale_f32_16x16x128_f8f6f4 v[86:89], v[2:9], v[198:205], v[86:89], v187, v188 op_sel_hi:[0,0,0]
	v_mfma_scale_f32_16x16x128_f8f6f4 v[78:81], v[10:17], v[198:205], v[78:81], v187, v188 op_sel_hi:[0,0,0]
	v_mfma_scale_f32_16x16x128_f8f6f4 v[70:73], v[2:9], v[206:213], v[70:73], v187, v188 op_sel_hi:[0,0,0]
	v_mfma_scale_f32_16x16x128_f8f6f4 v[62:65], v[10:17], v[206:213], v[62:65], v187, v188 op_sel_hi:[0,0,0]
	v_mfma_scale_f32_16x16x128_f8f6f4 v[54:57], v[2:9], v[220:227], v[54:57], v187, v188 op_sel_hi:[0,0,0]
	v_mfma_scale_f32_16x16x128_f8f6f4 v[46:49], v[10:17], v[220:227], v[46:49], v187, v188 op_sel_hi:[0,0,0]
	v_mfma_scale_f32_16x16x128_f8f6f4 v[82:85], v[18:25], v[190:197], v[82:85], v187, v188 op_sel_hi:[0,0,0]
	v_mfma_scale_f32_16x16x128_f8f6f4 v[74:77], v[26:33], v[190:197], v[74:77], v187, v188 op_sel_hi:[0,0,0]
	v_mfma_scale_f32_16x16x128_f8f6f4 v[66:69], v[18:25], v[198:205], v[66:69], v187, v188 op_sel_hi:[0,0,0]
	v_mfma_scale_f32_16x16x128_f8f6f4 v[58:61], v[26:33], v[198:205], v[58:61], v187, v188 op_sel_hi:[0,0,0]
	v_mfma_scale_f32_16x16x128_f8f6f4 v[50:53], v[18:25], v[206:213], v[50:53], v187, v188 op_sel_hi:[0,0,0]
	v_mfma_scale_f32_16x16x128_f8f6f4 v[42:45], v[26:33], v[206:213], v[42:45], v187, v188 op_sel_hi:[0,0,0]
	v_mfma_scale_f32_16x16x128_f8f6f4 v[38:41], v[18:25], v[220:227], v[38:41], v187, v188 op_sel_hi:[0,0,0]
	v_mfma_scale_f32_16x16x128_f8f6f4 v[34:37], v[26:33], v[220:227], v[34:37], v187, v188 op_sel_hi:[0,0,0]
	s_barrier
	s_add_i32 s94, s94, 2
	s_add_u32 s92, s92, 0x10000
	s_addc_u32 s93, s93, 0
	s_add_u32 s70, s70, 0x100
	s_addc_u32 s71, s71, 0
	s_cmp_gt_u32 s94, 13
	s_cbranch_scc0 .LBB0_285
	s_and_b64 vcc, exec, s[40:41]
	s_cbranch_vccz .LBB0_288
	s_barrier

.LBB0_660:
	ds_read_b128 v[130:133], v222
	ds_read_b128 v[134:137], v222 offset:1024
	ds_read_b128 v[138:141], v222 offset:2048
	ds_read_b128 v[142:145], v222 offset:3072
	ds_read_b128 v[146:149], v223
	ds_read_b128 v[150:153], v223 offset:1024
	ds_read_b128 v[154:157], v223 offset:2048
	ds_read_b128 v[158:161], v223 offset:3072
	s_add_u32 s26, s58, 0xfff80080
	s_addc_u32 s27, s59, -1
	s_cmp_eq_u32 s80, 28
	s_cselect_b32 s61, s45, s27
	s_cselect_b32 s60, s72, s26
	s_cselect_b32 s27, s41, s75
	s_cselect_b32 s26, s73, s74
	v_lshl_add_u64 v[208:209], s[58:59], 0, v[200:201]
	s_add_i32 m0, s57, 0xc000
	ds_read_b128 v[162:165], v224
	ds_read_b128 v[166:169], v224 offset:1024
	ds_read_b128 v[170:173], v224 offset:2048
	ds_read_b128 v[174:177], v224 offset:3072
	ds_read_b128 v[178:181], v224 offset:4096
	ds_read_b128 v[182:185], v224 offset:5120
	ds_read_b128 v[186:189], v224 offset:6144
	ds_read_b128 v[190:193], v224 offset:7168
	global_load_lds_dwordx4 v[208:209], off
	v_lshl_add_u64 v[208:209], s[58:59], 0, v[202:203]
	s_add_i32 m0, s57, 0xe000
	s_nop 0
	global_load_lds_dwordx4 v[208:209], off
	s_waitcnt vmcnt(8)
	s_waitcnt lgkmcnt(0)
	s_barrier
	s_waitcnt lgkmcnt(0)
	v_mfma_f32_16x16x32_bf16 v[126:129], v[130:133], v[162:165], v[126:129]
	v_mfma_f32_16x16x32_bf16 v[122:125], v[138:141], v[162:165], v[122:125]
	v_mfma_f32_16x16x32_bf16 v[118:121], v[130:133], v[170:173], v[118:121]
	v_mfma_f32_16x16x32_bf16 v[114:117], v[138:141], v[170:173], v[114:117]
	v_mfma_f32_16x16x32_bf16 v[110:113], v[130:133], v[178:181], v[110:113]
	v_mfma_f32_16x16x32_bf16 v[102:105], v[138:141], v[178:181], v[102:105]
	v_mfma_f32_16x16x32_bf16 v[94:97], v[130:133], v[186:189], v[94:97]
	v_mfma_f32_16x16x32_bf16 v[74:77], v[138:141], v[186:189], v[74:77]
	v_mfma_f32_16x16x32_bf16 v[126:129], v[134:137], v[166:169], v[126:129]
	v_mfma_f32_16x16x32_bf16 v[122:125], v[142:145], v[166:169], v[122:125]
	v_mfma_f32_16x16x32_bf16 v[118:121], v[134:137], v[174:177], v[118:121]
	v_mfma_f32_16x16x32_bf16 v[114:117], v[142:145], v[174:177], v[114:117]
	v_mfma_f32_16x16x32_bf16 v[110:113], v[134:137], v[182:185], v[110:113]
	v_mfma_f32_16x16x32_bf16 v[102:105], v[142:145], v[182:185], v[102:105]
	v_mfma_f32_16x16x32_bf16 v[94:97], v[134:137], v[190:193], v[94:97]
	v_mfma_f32_16x16x32_bf16 v[74:77], v[142:145], v[190:193], v[74:77]
	v_mfma_f32_16x16x32_bf16 v[106:109], v[146:149], v[162:165], v[106:109]
	v_mfma_f32_16x16x32_bf16 v[98:101], v[154:157], v[162:165], v[98:101]
	v_mfma_f32_16x16x32_bf16 v[90:93], v[146:149], v[170:173], v[90:93]
	v_mfma_f32_16x16x32_bf16 v[86:89], v[154:157], v[170:173], v[86:89]
	v_mfma_f32_16x16x32_bf16 v[82:85], v[146:149], v[178:181], v[82:85]
	v_mfma_f32_16x16x32_bf16 v[78:81], v[154:157], v[178:181], v[78:81]
	v_mfma_f32_16x16x32_bf16 v[70:73], v[146:149], v[186:189], v[70:73]
	v_mfma_f32_16x16x32_bf16 v[66:69], v[154:157], v[186:189], v[66:69]
	v_mfma_f32_16x16x32_bf16 v[106:109], v[150:153], v[166:169], v[106:109]
	v_mfma_f32_16x16x32_bf16 v[98:101], v[158:161], v[166:169], v[98:101]
	v_mfma_f32_16x16x32_bf16 v[90:93], v[150:153], v[174:177], v[90:93]
	v_mfma_f32_16x16x32_bf16 v[86:89], v[158:161], v[174:177], v[86:89]
	v_mfma_f32_16x16x32_bf16 v[82:85], v[150:153], v[182:185], v[82:85]
	v_mfma_f32_16x16x32_bf16 v[78:81], v[158:161], v[182:185], v[78:81]
	v_mfma_f32_16x16x32_bf16 v[70:73], v[150:153], v[190:193], v[70:73]
	v_mfma_f32_16x16x32_bf16 v[66:69], v[158:161], v[190:193], v[66:69]
	s_barrier
	v_lshl_add_u64 v[208:209], s[26:27], 0, v[194:195]
	s_add_i32 s26, s70, s35
	s_mov_b32 m0, s26
	ds_read_b128 v[162:165], v224 offset:16384
	ds_read_b128 v[166:169], v224 offset:17408
	ds_read_b128 v[170:173], v224 offset:18432
	ds_read_b128 v[174:177], v224 offset:19456
	ds_read_b128 v[178:181], v224 offset:20480
	ds_read_b128 v[182:185], v224 offset:21504
	ds_read_b128 v[186:189], v224 offset:22528
	ds_read_b128 v[190:193], v224 offset:23552
	global_load_lds_dwordx4 v[208:209], off
	v_lshl_add_u64 v[210:211], v[208:209], 0, s[6:7]
	s_add_i32 m0, s26, 0x2000
	s_add_i32 s26, s71, s35
	global_load_lds_dwordx4 v[210:211], off
	v_lshl_add_u64 v[210:211], v[208:209], 0, s[8:9]
	s_mov_b32 m0, s26
	v_lshl_add_u64 v[212:213], s[60:61], 0, v[198:199]
	global_load_lds_dwordx4 v[210:211], off
	v_lshl_add_u64 v[210:211], v[208:209], 0, s[10:11]
	s_add_i32 m0, s26, 0x2000
	s_nop 0
	global_load_lds_dwordx4 v[210:211], off
	v_lshl_add_u64 v[210:211], s[60:61], 0, v[196:197]
	s_mov_b32 m0, s57
	s_nop 0
	global_load_lds_dwordx4 v[210:211], off
	s_mov_b32 m0, s63
	s_nop 0
	global_load_lds_dwordx4 v[212:213], off
	s_waitcnt vmcnt(8)
	s_waitcnt lgkmcnt(0)
	s_barrier
	s_waitcnt lgkmcnt(0)
	v_mfma_f32_16x16x32_bf16 v[62:65], v[130:133], v[162:165], v[62:65]
	v_mfma_f32_16x16x32_bf16 v[58:61], v[138:141], v[162:165], v[58:61]
	v_mfma_f32_16x16x32_bf16 v[54:57], v[130:133], v[170:173], v[54:57]
	v_mfma_f32_16x16x32_bf16 v[50:53], v[138:141], v[170:173], v[50:53]
	v_mfma_f32_16x16x32_bf16 v[46:49], v[130:133], v[178:181], v[46:49]
	v_mfma_f32_16x16x32_bf16 v[38:41], v[138:141], v[178:181], v[38:41]
	v_mfma_f32_16x16x32_bf16 v[30:33], v[130:133], v[186:189], v[30:33]
	v_mfma_f32_16x16x32_bf16 v[10:13], v[138:141], v[186:189], v[10:13]
	v_mfma_f32_16x16x32_bf16 v[62:65], v[134:137], v[166:169], v[62:65]
	v_mfma_f32_16x16x32_bf16 v[58:61], v[142:145], v[166:169], v[58:61]
	v_mfma_f32_16x16x32_bf16 v[54:57], v[134:137], v[174:177], v[54:57]
	v_mfma_f32_16x16x32_bf16 v[50:53], v[142:145], v[174:177], v[50:53]
	v_mfma_f32_16x16x32_bf16 v[46:49], v[134:137], v[182:185], v[46:49]
	v_mfma_f32_16x16x32_bf16 v[38:41], v[142:145], v[182:185], v[38:41]
	v_mfma_f32_16x16x32_bf16 v[30:33], v[134:137], v[190:193], v[30:33]
	v_mfma_f32_16x16x32_bf16 v[10:13], v[142:145], v[190:193], v[10:13]
	v_mfma_f32_16x16x32_bf16 v[42:45], v[146:149], v[162:165], v[42:45]
	v_mfma_f32_16x16x32_bf16 v[34:37], v[154:157], v[162:165], v[34:37]
	v_mfma_f32_16x16x32_bf16 v[26:29], v[146:149], v[170:173], v[26:29]
	v_mfma_f32_16x16x32_bf16 v[22:25], v[154:157], v[170:173], v[22:25]
	v_mfma_f32_16x16x32_bf16 v[18:21], v[146:149], v[178:181], v[18:21]
	v_mfma_f32_16x16x32_bf16 v[14:17], v[154:157], v[178:181], v[14:17]
	v_mfma_f32_16x16x32_bf16 v[6:9], v[146:149], v[186:189], v[6:9]
	v_mfma_f32_16x16x32_bf16 v[2:5], v[154:157], v[186:189], v[2:5]
	v_mfma_f32_16x16x32_bf16 v[42:45], v[150:153], v[166:169], v[42:45]
	v_mfma_f32_16x16x32_bf16 v[34:37], v[158:161], v[166:169], v[34:37]
	v_mfma_f32_16x16x32_bf16 v[26:29], v[150:153], v[174:177], v[26:29]
	v_mfma_f32_16x16x32_bf16 v[22:25], v[158:161], v[174:177], v[22:25]
	v_mfma_f32_16x16x32_bf16 v[18:21], v[150:153], v[182:185], v[18:21]
	v_mfma_f32_16x16x32_bf16 v[14:17], v[158:161], v[182:185], v[14:17]
	v_mfma_f32_16x16x32_bf16 v[6:9], v[150:153], v[190:193], v[6:9]
	v_mfma_f32_16x16x32_bf16 v[2:5], v[158:161], v[190:193], v[2:5]
	s_barrier
	s_add_i32 s81, 0, 0x18000
	s_add_i32 s82, 0, 0x1c000
	v_add_u32_e32 v142, s81, v220
	v_add_u32_e32 v158, s82, v220
	ds_read_b128 v[130:133], v142
	ds_read_b128 v[134:137], v142 offset:1024
	ds_read_b128 v[138:141], v142 offset:2048
	ds_read_b128 v[142:145], v142 offset:3072
	ds_read_b128 v[146:149], v158
	ds_read_b128 v[150:153], v158 offset:1024
	ds_read_b128 v[154:157], v158 offset:2048
	ds_read_b128 v[158:161], v158 offset:3072
	s_add_u32 s26, s60, 0x80000
	s_addc_u32 s27, s61, 0
	s_mov_b32 m0, s64
	v_lshl_add_u64 v[214:215], s[26:27], 0, v[196:197]
	ds_read_b128 v[162:165], v224 offset:32768
	ds_read_b128 v[166:169], v224 offset:33792
	ds_read_b128 v[170:173], v224 offset:34816
	ds_read_b128 v[174:177], v224 offset:35840
	ds_read_b128 v[178:181], v224 offset:36864
	ds_read_b128 v[182:185], v224 offset:37888
	ds_read_b128 v[186:189], v224 offset:38912
	ds_read_b128 v[190:193], v224 offset:39936
	global_load_lds_dwordx4 v[214:215], off
	v_lshl_add_u64 v[214:215], s[26:27], 0, v[198:199]
	s_mov_b32 m0, s65
	s_nop 0
	global_load_lds_dwordx4 v[214:215], off
	s_waitcnt vmcnt(8)
	s_waitcnt lgkmcnt(0)
	s_barrier
	s_waitcnt lgkmcnt(0)
	v_mfma_f32_16x16x32_bf16 v[126:129], v[130:133], v[162:165], v[126:129]
	v_mfma_f32_16x16x32_bf16 v[122:125], v[138:141], v[162:165], v[122:125]
	v_mfma_f32_16x16x32_bf16 v[118:121], v[130:133], v[170:173], v[118:121]
	v_mfma_f32_16x16x32_bf16 v[114:117], v[138:141], v[170:173], v[114:117]
	v_mfma_f32_16x16x32_bf16 v[110:113], v[130:133], v[178:181], v[110:113]
	v_mfma_f32_16x16x32_bf16 v[102:105], v[138:141], v[178:181], v[102:105]
	v_mfma_f32_16x16x32_bf16 v[94:97], v[130:133], v[186:189], v[94:97]
	v_mfma_f32_16x16x32_bf16 v[74:77], v[138:141], v[186:189], v[74:77]
	v_mfma_f32_16x16x32_bf16 v[126:129], v[134:137], v[166:169], v[126:129]
	v_mfma_f32_16x16x32_bf16 v[122:125], v[142:145], v[166:169], v[122:125]
	v_mfma_f32_16x16x32_bf16 v[118:121], v[134:137], v[174:177], v[118:121]
	v_mfma_f32_16x16x32_bf16 v[114:117], v[142:145], v[174:177], v[114:117]
	v_mfma_f32_16x16x32_bf16 v[110:113], v[134:137], v[182:185], v[110:113]
	v_mfma_f32_16x16x32_bf16 v[102:105], v[142:145], v[182:185], v[102:105]
	v_mfma_f32_16x16x32_bf16 v[94:97], v[134:137], v[190:193], v[94:97]
	v_mfma_f32_16x16x32_bf16 v[74:77], v[142:145], v[190:193], v[74:77]
	v_mfma_f32_16x16x32_bf16 v[106:109], v[146:149], v[162:165], v[106:109]
	v_mfma_f32_16x16x32_bf16 v[98:101], v[154:157], v[162:165], v[98:101]
	v_mfma_f32_16x16x32_bf16 v[90:93], v[146:149], v[170:173], v[90:93]
	v_mfma_f32_16x16x32_bf16 v[86:89], v[154:157], v[170:173], v[86:89]
	v_mfma_f32_16x16x32_bf16 v[82:85], v[146:149], v[178:181], v[82:85]
	v_mfma_f32_16x16x32_bf16 v[78:81], v[154:157], v[178:181], v[78:81]
	v_mfma_f32_16x16x32_bf16 v[70:73], v[146:149], v[186:189], v[70:73]
	v_mfma_f32_16x16x32_bf16 v[66:69], v[154:157], v[186:189], v[66:69]
	v_mfma_f32_16x16x32_bf16 v[106:109], v[150:153], v[166:169], v[106:109]
	v_mfma_f32_16x16x32_bf16 v[98:101], v[158:161], v[166:169], v[98:101]
	v_mfma_f32_16x16x32_bf16 v[90:93], v[150:153], v[174:177], v[90:93]
	v_mfma_f32_16x16x32_bf16 v[86:89], v[158:161], v[174:177], v[86:89]
	v_mfma_f32_16x16x32_bf16 v[82:85], v[150:153], v[182:185], v[82:85]
	v_mfma_f32_16x16x32_bf16 v[78:81], v[158:161], v[182:185], v[78:81]
	v_mfma_f32_16x16x32_bf16 v[70:73], v[150:153], v[190:193], v[70:73]
	v_mfma_f32_16x16x32_bf16 v[66:69], v[158:161], v[190:193], v[66:69]
	s_barrier
	s_add_i32 s26, s81, s35
	v_lshl_add_u64 v[214:215], v[208:209], 0, s[14:15]
	s_mov_b32 m0, s26
	ds_read_b128 v[162:165], v224 offset:49152
	ds_read_b128 v[166:169], v224 offset:50176
	ds_read_b128 v[170:173], v224 offset:51200
	ds_read_b128 v[174:177], v224 offset:52224
	ds_read_b128 v[178:181], v224 offset:53248
	ds_read_b128 v[182:185], v224 offset:54272
	ds_read_b128 v[186:189], v224 offset:55296
	ds_read_b128 v[190:193], v224 offset:56320
	global_load_lds_dwordx4 v[214:215], off
	v_lshl_add_u64 v[214:215], v[208:209], 0, s[16:17]
	s_add_i32 m0, s26, 0x2000
	s_add_i32 s26, s82, s35
	global_load_lds_dwordx4 v[214:215], off
	v_lshl_add_u64 v[214:215], v[208:209], 0, s[20:21]
	s_mov_b32 m0, s26
	v_lshl_add_u64 v[208:209], v[208:209], 0, s[22:23]
	global_load_lds_dwordx4 v[214:215], off
	s_add_i32 m0, s26, 0x2000
	s_nop 0
	global_load_lds_dwordx4 v[208:209], off
	v_lshl_add_u64 v[208:209], v[210:211], 0, s[18:19]
	s_mov_b32 m0, s67
	s_nop 0
	global_load_lds_dwordx4 v[208:209], off
	v_lshl_add_u64 v[208:209], v[212:213], 0, s[18:19]
	s_mov_b32 m0, s68
	s_nop 0
	global_load_lds_dwordx4 v[208:209], off
	s_waitcnt vmcnt(8)
	s_waitcnt lgkmcnt(0)
	s_barrier
	s_waitcnt lgkmcnt(0)
	v_mfma_f32_16x16x32_bf16 v[62:65], v[130:133], v[162:165], v[62:65]
	v_mfma_f32_16x16x32_bf16 v[58:61], v[138:141], v[162:165], v[58:61]
	v_mfma_f32_16x16x32_bf16 v[54:57], v[130:133], v[170:173], v[54:57]
	v_mfma_f32_16x16x32_bf16 v[50:53], v[138:141], v[170:173], v[50:53]
	v_mfma_f32_16x16x32_bf16 v[46:49], v[130:133], v[178:181], v[46:49]
	v_mfma_f32_16x16x32_bf16 v[38:41], v[138:141], v[178:181], v[38:41]
	v_mfma_f32_16x16x32_bf16 v[30:33], v[130:133], v[186:189], v[30:33]
	v_mfma_f32_16x16x32_bf16 v[10:13], v[138:141], v[186:189], v[10:13]
	v_mfma_f32_16x16x32_bf16 v[62:65], v[134:137], v[166:169], v[62:65]
	v_mfma_f32_16x16x32_bf16 v[58:61], v[142:145], v[166:169], v[58:61]
	v_mfma_f32_16x16x32_bf16 v[54:57], v[134:137], v[174:177], v[54:57]
	v_mfma_f32_16x16x32_bf16 v[50:53], v[142:145], v[174:177], v[50:53]
	v_mfma_f32_16x16x32_bf16 v[46:49], v[134:137], v[182:185], v[46:49]
	v_mfma_f32_16x16x32_bf16 v[38:41], v[142:145], v[182:185], v[38:41]
	v_mfma_f32_16x16x32_bf16 v[30:33], v[134:137], v[190:193], v[30:33]
	v_mfma_f32_16x16x32_bf16 v[10:13], v[142:145], v[190:193], v[10:13]
	v_mfma_f32_16x16x32_bf16 v[42:45], v[146:149], v[162:165], v[42:45]
	v_mfma_f32_16x16x32_bf16 v[34:37], v[154:157], v[162:165], v[34:37]
	v_mfma_f32_16x16x32_bf16 v[26:29], v[146:149], v[170:173], v[26:29]
	v_mfma_f32_16x16x32_bf16 v[22:25], v[154:157], v[170:173], v[22:25]
	v_mfma_f32_16x16x32_bf16 v[18:21], v[146:149], v[178:181], v[18:21]
	v_mfma_f32_16x16x32_bf16 v[14:17], v[154:157], v[178:181], v[14:17]
	v_mfma_f32_16x16x32_bf16 v[6:9], v[146:149], v[186:189], v[6:9]
	v_mfma_f32_16x16x32_bf16 v[2:5], v[154:157], v[186:189], v[2:5]
	v_mfma_f32_16x16x32_bf16 v[42:45], v[150:153], v[166:169], v[42:45]
	v_mfma_f32_16x16x32_bf16 v[34:37], v[158:161], v[166:169], v[34:37]
	v_mfma_f32_16x16x32_bf16 v[26:29], v[150:153], v[174:177], v[26:29]
	v_mfma_f32_16x16x32_bf16 v[22:25], v[158:161], v[174:177], v[22:25]
	v_mfma_f32_16x16x32_bf16 v[18:21], v[150:153], v[182:185], v[18:21]
	v_mfma_f32_16x16x32_bf16 v[14:17], v[158:161], v[182:185], v[14:17]
	v_mfma_f32_16x16x32_bf16 v[6:9], v[150:153], v[190:193], v[6:9]
	v_mfma_f32_16x16x32_bf16 v[2:5], v[158:161], v[190:193], v[2:5]
	s_barrier
	s_add_i32 s80, s80, 2
	s_add_u32 s74, s74, 0x10000
	s_addc_u32 s75, s75, 0
	s_add_u32 s58, s58, 0x100
	s_addc_u32 s59, s59, 0
	s_cmp_gt_u32 s80, 29
	s_cbranch_scc0 .LBB0_660
	s_and_b64 vcc, exec, s[24:25]
	s_cbranch_vccz .LBB0_663
	s_barrier

.LBB0_783:
	ds_read_b128 v[144:147], v151
	ds_read_b128 v[156:159], v151 offset:1024
	ds_read_b128 v[160:163], v151 offset:2048
	ds_read_b128 v[164:167], v151 offset:3072
	ds_read_b128 v[168:171], v152
	ds_read_b128 v[172:175], v152 offset:1024
	ds_read_b128 v[176:179], v152 offset:2048
	ds_read_b128 v[180:183], v152 offset:3072
	s_add_u32 s26, s62, 0xfff80080
	s_addc_u32 s27, s63, -1
	s_cmp_eq_u32 s85, 28
	s_cselect_b32 s65, s55, s27
	s_cselect_b32 s64, s81, s26
	s_cselect_b32 s27, s53, s84
	s_cselect_b32 s26, s82, s83
	v_lshl_add_u64 v[216:217], s[62:63], 0, v[136:137]
	s_add_i32 m0, s61, 0xc000
	ds_read_b128 v[184:187], v153
	ds_read_b128 v[188:191], v153 offset:1024
	ds_read_b128 v[192:195], v153 offset:2048
	ds_read_b128 v[196:199], v153 offset:3072
	ds_read_b128 v[200:203], v153 offset:4096
	ds_read_b128 v[204:207], v153 offset:5120
	ds_read_b128 v[208:211], v153 offset:6144
	ds_read_b128 v[212:215], v153 offset:7168
	global_load_lds_dwordx4 v[216:217], off
	v_lshl_add_u64 v[216:217], s[62:63], 0, v[138:139]
	s_add_i32 m0, s61, 0xe000
	s_nop 0
	global_load_lds_dwordx4 v[216:217], off
	s_waitcnt vmcnt(8)
	s_waitcnt lgkmcnt(0)
	s_barrier
	s_waitcnt lgkmcnt(0)
	v_mfma_f32_16x16x32_bf16 v[126:129], v[144:147], v[184:187], v[126:129]
	v_mfma_f32_16x16x32_bf16 v[118:121], v[160:163], v[184:187], v[118:121]
	v_mfma_f32_16x16x32_bf16 v[110:113], v[144:147], v[192:195], v[110:113]
	v_mfma_f32_16x16x32_bf16 v[102:105], v[160:163], v[192:195], v[102:105]
	v_mfma_f32_16x16x32_bf16 v[94:97], v[144:147], v[200:203], v[94:97]
	v_mfma_f32_16x16x32_bf16 v[86:89], v[160:163], v[200:203], v[86:89]
	v_mfma_f32_16x16x32_bf16 v[78:81], v[144:147], v[208:211], v[78:81]
	v_mfma_f32_16x16x32_bf16 v[70:73], v[160:163], v[208:211], v[70:73]
	v_mfma_f32_16x16x32_bf16 v[126:129], v[156:159], v[188:191], v[126:129]
	v_mfma_f32_16x16x32_bf16 v[118:121], v[164:167], v[188:191], v[118:121]
	v_mfma_f32_16x16x32_bf16 v[110:113], v[156:159], v[196:199], v[110:113]
	v_mfma_f32_16x16x32_bf16 v[102:105], v[164:167], v[196:199], v[102:105]
	v_mfma_f32_16x16x32_bf16 v[94:97], v[156:159], v[204:207], v[94:97]
	v_mfma_f32_16x16x32_bf16 v[86:89], v[164:167], v[204:207], v[86:89]
	v_mfma_f32_16x16x32_bf16 v[78:81], v[156:159], v[212:215], v[78:81]
	v_mfma_f32_16x16x32_bf16 v[70:73], v[164:167], v[212:215], v[70:73]
	v_mfma_f32_16x16x32_bf16 v[122:125], v[168:171], v[184:187], v[122:125]
	v_mfma_f32_16x16x32_bf16 v[114:117], v[176:179], v[184:187], v[114:117]
	v_mfma_f32_16x16x32_bf16 v[106:109], v[168:171], v[192:195], v[106:109]
	v_mfma_f32_16x16x32_bf16 v[98:101], v[176:179], v[192:195], v[98:101]
	v_mfma_f32_16x16x32_bf16 v[90:93], v[168:171], v[200:203], v[90:93]
	v_mfma_f32_16x16x32_bf16 v[82:85], v[176:179], v[200:203], v[82:85]
	v_mfma_f32_16x16x32_bf16 v[74:77], v[168:171], v[208:211], v[74:77]
	v_mfma_f32_16x16x32_bf16 v[66:69], v[176:179], v[208:211], v[66:69]
	v_mfma_f32_16x16x32_bf16 v[122:125], v[172:175], v[188:191], v[122:125]
	v_mfma_f32_16x16x32_bf16 v[114:117], v[180:183], v[188:191], v[114:117]
	v_mfma_f32_16x16x32_bf16 v[106:109], v[172:175], v[196:199], v[106:109]
	v_mfma_f32_16x16x32_bf16 v[98:101], v[180:183], v[196:199], v[98:101]
	v_mfma_f32_16x16x32_bf16 v[90:93], v[172:175], v[204:207], v[90:93]
	v_mfma_f32_16x16x32_bf16 v[82:85], v[180:183], v[204:207], v[82:85]
	v_mfma_f32_16x16x32_bf16 v[74:77], v[172:175], v[212:215], v[74:77]
	v_mfma_f32_16x16x32_bf16 v[66:69], v[180:183], v[212:215], v[66:69]
	s_barrier
	v_lshl_add_u64 v[216:217], s[26:27], 0, v[130:131]
	s_add_i32 s26, s73, s35
	s_mov_b32 m0, s26
	ds_read_b128 v[184:187], v153 offset:16384
	ds_read_b128 v[188:191], v153 offset:17408
	ds_read_b128 v[192:195], v153 offset:18432
	ds_read_b128 v[196:199], v153 offset:19456
	ds_read_b128 v[200:203], v153 offset:20480
	ds_read_b128 v[204:207], v153 offset:21504
	ds_read_b128 v[208:211], v153 offset:22528
	ds_read_b128 v[212:215], v153 offset:23552
	global_load_lds_dwordx4 v[216:217], off
	v_lshl_add_u64 v[220:221], v[216:217], 0, s[6:7]
	s_add_i32 m0, s26, 0x2000
	s_add_i32 s26, s74, s35
	global_load_lds_dwordx4 v[220:221], off
	v_lshl_add_u64 v[220:221], v[216:217], 0, s[8:9]
	s_mov_b32 m0, s26
	v_lshl_add_u64 v[222:223], s[64:65], 0, v[134:135]
	global_load_lds_dwordx4 v[220:221], off
	v_lshl_add_u64 v[220:221], v[216:217], 0, s[10:11]
	s_add_i32 m0, s26, 0x2000
	s_nop 0
	global_load_lds_dwordx4 v[220:221], off
	v_lshl_add_u64 v[220:221], s[64:65], 0, v[132:133]
	s_mov_b32 m0, s61
	s_nop 0
	global_load_lds_dwordx4 v[220:221], off
	s_mov_b32 m0, s66
	s_nop 0
	global_load_lds_dwordx4 v[222:223], off
	s_waitcnt vmcnt(8)
	s_waitcnt lgkmcnt(0)
	s_barrier
	s_waitcnt lgkmcnt(0)
	v_mfma_f32_16x16x32_bf16 v[62:65], v[144:147], v[184:187], v[62:65]
	v_mfma_f32_16x16x32_bf16 v[54:57], v[160:163], v[184:187], v[54:57]
	v_mfma_f32_16x16x32_bf16 v[46:49], v[144:147], v[192:195], v[46:49]
	v_mfma_f32_16x16x32_bf16 v[38:41], v[160:163], v[192:195], v[38:41]
	v_mfma_f32_16x16x32_bf16 v[30:33], v[144:147], v[200:203], v[30:33]
	v_mfma_f32_16x16x32_bf16 v[22:25], v[160:163], v[200:203], v[22:25]
	v_mfma_f32_16x16x32_bf16 v[14:17], v[144:147], v[208:211], v[14:17]
	v_mfma_f32_16x16x32_bf16 v[6:9], v[160:163], v[208:211], v[6:9]
	v_mfma_f32_16x16x32_bf16 v[62:65], v[156:159], v[188:191], v[62:65]
	v_mfma_f32_16x16x32_bf16 v[54:57], v[164:167], v[188:191], v[54:57]
	v_mfma_f32_16x16x32_bf16 v[46:49], v[156:159], v[196:199], v[46:49]
	v_mfma_f32_16x16x32_bf16 v[38:41], v[164:167], v[196:199], v[38:41]
	v_mfma_f32_16x16x32_bf16 v[30:33], v[156:159], v[204:207], v[30:33]
	v_mfma_f32_16x16x32_bf16 v[22:25], v[164:167], v[204:207], v[22:25]
	v_mfma_f32_16x16x32_bf16 v[14:17], v[156:159], v[212:215], v[14:17]
	v_mfma_f32_16x16x32_bf16 v[6:9], v[164:167], v[212:215], v[6:9]
	v_mfma_f32_16x16x32_bf16 v[58:61], v[168:171], v[184:187], v[58:61]
	v_mfma_f32_16x16x32_bf16 v[50:53], v[176:179], v[184:187], v[50:53]
	v_mfma_f32_16x16x32_bf16 v[42:45], v[168:171], v[192:195], v[42:45]
	v_mfma_f32_16x16x32_bf16 v[34:37], v[176:179], v[192:195], v[34:37]
	v_mfma_f32_16x16x32_bf16 v[26:29], v[168:171], v[200:203], v[26:29]
	v_mfma_f32_16x16x32_bf16 v[18:21], v[176:179], v[200:203], v[18:21]
	v_mfma_f32_16x16x32_bf16 v[10:13], v[168:171], v[208:211], v[10:13]
	v_mfma_f32_16x16x32_bf16 v[2:5], v[176:179], v[208:211], v[2:5]
	v_mfma_f32_16x16x32_bf16 v[58:61], v[172:175], v[188:191], v[58:61]
	v_mfma_f32_16x16x32_bf16 v[50:53], v[180:183], v[188:191], v[50:53]
	v_mfma_f32_16x16x32_bf16 v[42:45], v[172:175], v[196:199], v[42:45]
	v_mfma_f32_16x16x32_bf16 v[34:37], v[180:183], v[196:199], v[34:37]
	v_mfma_f32_16x16x32_bf16 v[26:29], v[172:175], v[204:207], v[26:29]
	v_mfma_f32_16x16x32_bf16 v[18:21], v[180:183], v[204:207], v[18:21]
	v_mfma_f32_16x16x32_bf16 v[10:13], v[172:175], v[212:215], v[10:13]
	v_mfma_f32_16x16x32_bf16 v[2:5], v[180:183], v[212:215], v[2:5]
	s_barrier
	s_add_i32 s86, 0, 0x18000
	v_add_u32_e32 v155, s86, v149
	s_add_i32 s87, 0, 0x1c000
	ds_read_b128 v[144:147], v155
	ds_read_b128 v[156:159], v155 offset:1024
	ds_read_b128 v[160:163], v155 offset:2048
	ds_read_b128 v[164:167], v155 offset:3072
	v_add_u32_e32 v155, s87, v149
	ds_read_b128 v[168:171], v155
	ds_read_b128 v[172:175], v155 offset:1024
	ds_read_b128 v[176:179], v155 offset:2048
	ds_read_b128 v[180:183], v155 offset:3072
	s_add_u32 s26, s64, 0x80000
	s_addc_u32 s27, s65, 0
	s_mov_b32 m0, s67
	v_lshl_add_u64 v[224:225], s[26:27], 0, v[132:133]
	ds_read_b128 v[184:187], v153 offset:32768
	ds_read_b128 v[188:191], v153 offset:33792
	ds_read_b128 v[192:195], v153 offset:34816
	ds_read_b128 v[196:199], v153 offset:35840
	ds_read_b128 v[200:203], v153 offset:36864
	ds_read_b128 v[204:207], v153 offset:37888
	ds_read_b128 v[208:211], v153 offset:38912
	ds_read_b128 v[212:215], v153 offset:39936
	global_load_lds_dwordx4 v[224:225], off
	v_lshl_add_u64 v[224:225], s[26:27], 0, v[134:135]
	s_mov_b32 m0, s68
	s_nop 0
	global_load_lds_dwordx4 v[224:225], off
	s_waitcnt vmcnt(8)
	s_waitcnt lgkmcnt(0)
	s_barrier
	s_waitcnt lgkmcnt(0)
	v_mfma_f32_16x16x32_bf16 v[126:129], v[144:147], v[184:187], v[126:129]
	v_mfma_f32_16x16x32_bf16 v[118:121], v[160:163], v[184:187], v[118:121]
	v_mfma_f32_16x16x32_bf16 v[110:113], v[144:147], v[192:195], v[110:113]
	v_mfma_f32_16x16x32_bf16 v[102:105], v[160:163], v[192:195], v[102:105]
	v_mfma_f32_16x16x32_bf16 v[94:97], v[144:147], v[200:203], v[94:97]
	v_mfma_f32_16x16x32_bf16 v[86:89], v[160:163], v[200:203], v[86:89]
	v_mfma_f32_16x16x32_bf16 v[78:81], v[144:147], v[208:211], v[78:81]
	v_mfma_f32_16x16x32_bf16 v[70:73], v[160:163], v[208:211], v[70:73]
	v_mfma_f32_16x16x32_bf16 v[126:129], v[156:159], v[188:191], v[126:129]
	v_mfma_f32_16x16x32_bf16 v[118:121], v[164:167], v[188:191], v[118:121]
	v_mfma_f32_16x16x32_bf16 v[110:113], v[156:159], v[196:199], v[110:113]
	v_mfma_f32_16x16x32_bf16 v[102:105], v[164:167], v[196:199], v[102:105]
	v_mfma_f32_16x16x32_bf16 v[94:97], v[156:159], v[204:207], v[94:97]
	v_mfma_f32_16x16x32_bf16 v[86:89], v[164:167], v[204:207], v[86:89]
	v_mfma_f32_16x16x32_bf16 v[78:81], v[156:159], v[212:215], v[78:81]
	v_mfma_f32_16x16x32_bf16 v[70:73], v[164:167], v[212:215], v[70:73]
	v_mfma_f32_16x16x32_bf16 v[122:125], v[168:171], v[184:187], v[122:125]
	v_mfma_f32_16x16x32_bf16 v[114:117], v[176:179], v[184:187], v[114:117]
	v_mfma_f32_16x16x32_bf16 v[106:109], v[168:171], v[192:195], v[106:109]
	v_mfma_f32_16x16x32_bf16 v[98:101], v[176:179], v[192:195], v[98:101]
	v_mfma_f32_16x16x32_bf16 v[90:93], v[168:171], v[200:203], v[90:93]
	v_mfma_f32_16x16x32_bf16 v[82:85], v[176:179], v[200:203], v[82:85]
	v_mfma_f32_16x16x32_bf16 v[74:77], v[168:171], v[208:211], v[74:77]
	v_mfma_f32_16x16x32_bf16 v[66:69], v[176:179], v[208:211], v[66:69]
	v_mfma_f32_16x16x32_bf16 v[122:125], v[172:175], v[188:191], v[122:125]
	v_mfma_f32_16x16x32_bf16 v[114:117], v[180:183], v[188:191], v[114:117]
	v_mfma_f32_16x16x32_bf16 v[106:109], v[172:175], v[196:199], v[106:109]
	v_mfma_f32_16x16x32_bf16 v[98:101], v[180:183], v[196:199], v[98:101]
	v_mfma_f32_16x16x32_bf16 v[90:93], v[172:175], v[204:207], v[90:93]
	v_mfma_f32_16x16x32_bf16 v[82:85], v[180:183], v[204:207], v[82:85]
	v_mfma_f32_16x16x32_bf16 v[74:77], v[172:175], v[212:215], v[74:77]
	v_mfma_f32_16x16x32_bf16 v[66:69], v[180:183], v[212:215], v[66:69]
	s_barrier
	s_add_i32 s26, s86, s35
	v_lshl_add_u64 v[224:225], v[216:217], 0, s[16:17]
	s_mov_b32 m0, s26
	ds_read_b128 v[184:187], v153 offset:49152
	ds_read_b128 v[188:191], v153 offset:50176
	ds_read_b128 v[192:195], v153 offset:51200
	ds_read_b128 v[196:199], v153 offset:52224
	ds_read_b128 v[200:203], v153 offset:53248
	ds_read_b128 v[204:207], v153 offset:54272
	ds_read_b128 v[208:211], v153 offset:55296
	ds_read_b128 v[212:215], v153 offset:56320
	global_load_lds_dwordx4 v[224:225], off
	v_lshl_add_u64 v[224:225], v[216:217], 0, s[18:19]
	s_add_i32 m0, s26, 0x2000
	s_add_i32 s26, s87, s35
	global_load_lds_dwordx4 v[224:225], off
	v_lshl_add_u64 v[224:225], v[216:217], 0, s[22:23]
	s_mov_b32 m0, s26
	v_lshl_add_u64 v[216:217], v[216:217], 0, s[24:25]
	global_load_lds_dwordx4 v[224:225], off
	s_add_i32 m0, s26, 0x2000
	s_nop 0
	global_load_lds_dwordx4 v[216:217], off
	v_lshl_add_u64 v[216:217], v[220:221], 0, s[20:21]
	s_mov_b32 m0, s70
	s_nop 0
	global_load_lds_dwordx4 v[216:217], off
	v_lshl_add_u64 v[216:217], v[222:223], 0, s[20:21]
	s_mov_b32 m0, s71
	s_nop 0
	global_load_lds_dwordx4 v[216:217], off
	s_waitcnt vmcnt(8)
	s_waitcnt lgkmcnt(0)
	s_barrier
	s_waitcnt lgkmcnt(0)
	v_mfma_f32_16x16x32_bf16 v[62:65], v[144:147], v[184:187], v[62:65]
	v_mfma_f32_16x16x32_bf16 v[54:57], v[160:163], v[184:187], v[54:57]
	v_mfma_f32_16x16x32_bf16 v[46:49], v[144:147], v[192:195], v[46:49]
	v_mfma_f32_16x16x32_bf16 v[38:41], v[160:163], v[192:195], v[38:41]
	v_mfma_f32_16x16x32_bf16 v[30:33], v[144:147], v[200:203], v[30:33]
	v_mfma_f32_16x16x32_bf16 v[22:25], v[160:163], v[200:203], v[22:25]
	v_mfma_f32_16x16x32_bf16 v[14:17], v[144:147], v[208:211], v[14:17]
	v_mfma_f32_16x16x32_bf16 v[6:9], v[160:163], v[208:211], v[6:9]
	v_mfma_f32_16x16x32_bf16 v[62:65], v[156:159], v[188:191], v[62:65]
	v_mfma_f32_16x16x32_bf16 v[54:57], v[164:167], v[188:191], v[54:57]
	v_mfma_f32_16x16x32_bf16 v[46:49], v[156:159], v[196:199], v[46:49]
	v_mfma_f32_16x16x32_bf16 v[38:41], v[164:167], v[196:199], v[38:41]
	v_mfma_f32_16x16x32_bf16 v[30:33], v[156:159], v[204:207], v[30:33]
	v_mfma_f32_16x16x32_bf16 v[22:25], v[164:167], v[204:207], v[22:25]
	v_mfma_f32_16x16x32_bf16 v[14:17], v[156:159], v[212:215], v[14:17]
	v_mfma_f32_16x16x32_bf16 v[6:9], v[164:167], v[212:215], v[6:9]
	v_mfma_f32_16x16x32_bf16 v[58:61], v[168:171], v[184:187], v[58:61]
	v_mfma_f32_16x16x32_bf16 v[50:53], v[176:179], v[184:187], v[50:53]
	v_mfma_f32_16x16x32_bf16 v[42:45], v[168:171], v[192:195], v[42:45]
	v_mfma_f32_16x16x32_bf16 v[34:37], v[176:179], v[192:195], v[34:37]
	v_mfma_f32_16x16x32_bf16 v[26:29], v[168:171], v[200:203], v[26:29]
	v_mfma_f32_16x16x32_bf16 v[18:21], v[176:179], v[200:203], v[18:21]
	v_mfma_f32_16x16x32_bf16 v[10:13], v[168:171], v[208:211], v[10:13]
	v_mfma_f32_16x16x32_bf16 v[2:5], v[176:179], v[208:211], v[2:5]
	v_mfma_f32_16x16x32_bf16 v[58:61], v[172:175], v[188:191], v[58:61]
	v_mfma_f32_16x16x32_bf16 v[50:53], v[180:183], v[188:191], v[50:53]
	v_mfma_f32_16x16x32_bf16 v[42:45], v[172:175], v[196:199], v[42:45]
	v_mfma_f32_16x16x32_bf16 v[34:37], v[180:183], v[196:199], v[34:37]
	v_mfma_f32_16x16x32_bf16 v[26:29], v[172:175], v[204:207], v[26:29]
	v_mfma_f32_16x16x32_bf16 v[18:21], v[180:183], v[204:207], v[18:21]
	v_mfma_f32_16x16x32_bf16 v[10:13], v[172:175], v[212:215], v[10:13]
	v_mfma_f32_16x16x32_bf16 v[2:5], v[180:183], v[212:215], v[2:5]
	s_barrier
	s_add_i32 s85, s85, 2
	s_add_u32 s83, s83, 0x10000
	s_addc_u32 s84, s84, 0
	s_add_u32 s62, s62, 0x100
	s_addc_u32 s63, s63, 0
	s_cmp_gt_u32 s85, 29
	s_cbranch_scc0 .LBB0_783
	s_and_b64 vcc, exec, s[40:41]
	s_cbranch_vccz .LBB0_786
	s_barrier

.LBB0_858:
	ds_read_b128 v[26:29], v185
	ds_read_b128 v[30:33], v185 offset:1024
	ds_read_b128 v[18:21], v185 offset:2048
	ds_read_b128 v[22:25], v185 offset:3072
	ds_read_b128 v[10:13], v186
	ds_read_b128 v[14:17], v186 offset:1024
	ds_read_b128 v[2:5], v186 offset:2048
	ds_read_b128 v[6:9], v186 offset:3072
	s_add_u32 s26, s50, 0xfff50080
	s_addc_u32 s27, s51, -1
	s_cmp_eq_u32 s74, 40
	s_cselect_b32 s53, s5, s27
	s_cselect_b32 s52, s4, s26
	s_cselect_b32 s55, s45, s73
	s_cselect_b32 s54, s44, s72
	v_lshl_add_u64 v[176:177], s[50:51], 0, v[168:169]
	s_add_i32 m0, s59, 0xc000
	ds_read_b128 v[190:193], v187
	ds_read_b128 v[194:197], v187 offset:1024
	ds_read_b128 v[198:201], v187 offset:2048
	ds_read_b128 v[202:205], v187 offset:3072
	ds_read_b128 v[206:209], v187 offset:4096
	ds_read_b128 v[210:213], v187 offset:5120
	ds_read_b128 v[220:223], v187 offset:6144
	ds_read_b128 v[224:227], v187 offset:7168
	global_load_lds_dwordx4 v[176:177], off
	v_lshl_add_u64 v[176:177], s[50:51], 0, v[170:171]
	s_add_i32 m0, s59, 0xe000
	s_nop 0
	global_load_lds_dwordx4 v[176:177], off
	s_waitcnt vmcnt(8)
	s_waitcnt lgkmcnt(0)
	s_barrier
	s_waitcnt lgkmcnt(0)
	v_mfma_scale_f32_16x16x128_f8f6f4 v[158:161], v[26:33], v[190:197], v[158:161], v188, v189 op_sel_hi:[0,0,0]
	v_mfma_scale_f32_16x16x128_f8f6f4 v[154:157], v[18:25], v[190:197], v[154:157], v188, v189 op_sel_hi:[0,0,0]
	v_mfma_scale_f32_16x16x128_f8f6f4 v[150:153], v[26:33], v[198:205], v[150:153], v188, v189 op_sel_hi:[0,0,0]
	v_mfma_scale_f32_16x16x128_f8f6f4 v[146:149], v[18:25], v[198:205], v[146:149], v188, v189 op_sel_hi:[0,0,0]
	v_mfma_scale_f32_16x16x128_f8f6f4 v[138:141], v[26:33], v[206:213], v[138:141], v188, v189 op_sel_hi:[0,0,0]
	v_mfma_scale_f32_16x16x128_f8f6f4 v[130:133], v[18:25], v[206:213], v[130:133], v188, v189 op_sel_hi:[0,0,0]
	v_mfma_scale_f32_16x16x128_f8f6f4 v[122:125], v[26:33], v[220:227], v[122:125], v188, v189 op_sel_hi:[0,0,0]
	v_mfma_scale_f32_16x16x128_f8f6f4 v[114:117], v[18:25], v[220:227], v[114:117], v188, v189 op_sel_hi:[0,0,0]
	v_mfma_scale_f32_16x16x128_f8f6f4 v[142:145], v[10:17], v[190:197], v[142:145], v188, v189 op_sel_hi:[0,0,0]
	v_mfma_scale_f32_16x16x128_f8f6f4 v[134:137], v[2:9], v[190:197], v[134:137], v188, v189 op_sel_hi:[0,0,0]
	v_mfma_scale_f32_16x16x128_f8f6f4 v[126:129], v[10:17], v[198:205], v[126:129], v188, v189 op_sel_hi:[0,0,0]
	v_mfma_scale_f32_16x16x128_f8f6f4 v[118:121], v[2:9], v[198:205], v[118:121], v188, v189 op_sel_hi:[0,0,0]
	v_mfma_scale_f32_16x16x128_f8f6f4 v[110:113], v[10:17], v[206:213], v[110:113], v188, v189 op_sel_hi:[0,0,0]
	v_mfma_scale_f32_16x16x128_f8f6f4 v[106:109], v[2:9], v[206:213], v[106:109], v188, v189 op_sel_hi:[0,0,0]
	v_mfma_scale_f32_16x16x128_f8f6f4 v[102:105], v[10:17], v[220:227], v[102:105], v188, v189 op_sel_hi:[0,0,0]
	v_mfma_scale_f32_16x16x128_f8f6f4 v[98:101], v[2:9], v[220:227], v[98:101], v188, v189 op_sel_hi:[0,0,0]
	s_barrier
	s_add_i32 s26, s67, s57
	v_lshl_add_u64 v[176:177], s[54:55], 0, v[162:163]
	s_mov_b32 m0, s26
	ds_read_b128 v[190:193], v187 offset:16384
	ds_read_b128 v[194:197], v187 offset:17408
	ds_read_b128 v[198:201], v187 offset:18432
	ds_read_b128 v[202:205], v187 offset:19456
	ds_read_b128 v[206:209], v187 offset:20480
	ds_read_b128 v[210:213], v187 offset:21504
	ds_read_b128 v[220:223], v187 offset:22528
	ds_read_b128 v[224:227], v187 offset:23552
	global_load_lds_dwordx4 v[176:177], off
	v_lshl_add_u64 v[178:179], v[176:177], 0, s[8:9]
	s_add_i32 m0, s26, 0x2000
	s_add_i32 s26, s68, s57
	global_load_lds_dwordx4 v[178:179], off
	v_lshl_add_u64 v[178:179], v[176:177], 0, s[10:11]
	s_mov_b32 m0, s26
	v_lshl_add_u64 v[180:181], s[52:53], 0, v[166:167]
	global_load_lds_dwordx4 v[178:179], off
	v_lshl_add_u64 v[178:179], v[176:177], 0, s[12:13]
	s_add_i32 m0, s26, 0x2000
	s_nop 0
	global_load_lds_dwordx4 v[178:179], off
	v_lshl_add_u64 v[178:179], s[52:53], 0, v[164:165]
	s_mov_b32 m0, s59
	s_nop 0
	global_load_lds_dwordx4 v[178:179], off
	s_mov_b32 m0, s60
	s_nop 0
	global_load_lds_dwordx4 v[180:181], off
	s_waitcnt vmcnt(8)
	s_waitcnt lgkmcnt(0)
	s_barrier
	s_waitcnt lgkmcnt(0)
	v_mfma_scale_f32_16x16x128_f8f6f4 v[94:97], v[26:33], v[190:197], v[94:97], v188, v189 op_sel_hi:[0,0,0]
	v_mfma_scale_f32_16x16x128_f8f6f4 v[90:93], v[18:25], v[190:197], v[90:93], v188, v189 op_sel_hi:[0,0,0]
	v_mfma_scale_f32_16x16x128_f8f6f4 v[86:89], v[26:33], v[198:205], v[86:89], v188, v189 op_sel_hi:[0,0,0]
	v_mfma_scale_f32_16x16x128_f8f6f4 v[78:81], v[18:25], v[198:205], v[78:81], v188, v189 op_sel_hi:[0,0,0]
	v_mfma_scale_f32_16x16x128_f8f6f4 v[70:73], v[26:33], v[206:213], v[70:73], v188, v189 op_sel_hi:[0,0,0]
	v_mfma_scale_f32_16x16x128_f8f6f4 v[62:65], v[18:25], v[206:213], v[62:65], v188, v189 op_sel_hi:[0,0,0]
	v_mfma_scale_f32_16x16x128_f8f6f4 v[54:57], v[26:33], v[220:227], v[54:57], v188, v189 op_sel_hi:[0,0,0]
	v_mfma_scale_f32_16x16x128_f8f6f4 v[46:49], v[18:25], v[220:227], v[46:49], v188, v189 op_sel_hi:[0,0,0]
	v_mfma_scale_f32_16x16x128_f8f6f4 v[82:85], v[10:17], v[190:197], v[82:85], v188, v189 op_sel_hi:[0,0,0]
	v_mfma_scale_f32_16x16x128_f8f6f4 v[74:77], v[2:9], v[190:197], v[74:77], v188, v189 op_sel_hi:[0,0,0]
	v_mfma_scale_f32_16x16x128_f8f6f4 v[66:69], v[10:17], v[198:205], v[66:69], v188, v189 op_sel_hi:[0,0,0]
	v_mfma_scale_f32_16x16x128_f8f6f4 v[58:61], v[2:9], v[198:205], v[58:61], v188, v189 op_sel_hi:[0,0,0]
	v_mfma_scale_f32_16x16x128_f8f6f4 v[50:53], v[10:17], v[206:213], v[50:53], v188, v189 op_sel_hi:[0,0,0]
	v_mfma_scale_f32_16x16x128_f8f6f4 v[42:45], v[2:9], v[206:213], v[42:45], v188, v189 op_sel_hi:[0,0,0]
	v_mfma_scale_f32_16x16x128_f8f6f4 v[38:41], v[10:17], v[220:227], v[38:41], v188, v189 op_sel_hi:[0,0,0]
	v_mfma_scale_f32_16x16x128_f8f6f4 v[34:37], v[2:9], v[220:227], v[34:37], v188, v189 op_sel_hi:[0,0,0]
	s_barrier
	s_add_i32 s54, 0, 0x18000
	s_add_i32 s55, 0, 0x1c000
	v_add_u32_e32 v14, s54, v183
	v_add_u32_e32 v30, s55, v183
	ds_read_b128 v[2:5], v14
	ds_read_b128 v[6:9], v14 offset:1024
	ds_read_b128 v[10:13], v14 offset:2048
	ds_read_b128 v[14:17], v14 offset:3072
	ds_read_b128 v[18:21], v30
	ds_read_b128 v[22:25], v30 offset:1024
	ds_read_b128 v[26:29], v30 offset:2048
	ds_read_b128 v[30:33], v30 offset:3072
	s_add_u32 s26, s52, 0xb0000
	s_addc_u32 s27, s53, 0
	s_mov_b32 m0, s61
	v_lshl_add_u64 v[214:215], s[26:27], 0, v[164:165]
	ds_read_b128 v[190:193], v187 offset:32768
	ds_read_b128 v[194:197], v187 offset:33792
	ds_read_b128 v[198:201], v187 offset:34816
	ds_read_b128 v[202:205], v187 offset:35840
	ds_read_b128 v[206:209], v187 offset:36864
	ds_read_b128 v[210:213], v187 offset:37888
	ds_read_b128 v[220:223], v187 offset:38912
	ds_read_b128 v[224:227], v187 offset:39936
	global_load_lds_dwordx4 v[214:215], off
	v_lshl_add_u64 v[214:215], s[26:27], 0, v[166:167]
	s_mov_b32 m0, s62
	s_nop 0
	global_load_lds_dwordx4 v[214:215], off
	s_waitcnt vmcnt(8)
	s_waitcnt lgkmcnt(0)
	s_barrier
	s_waitcnt lgkmcnt(0)
	v_mfma_scale_f32_16x16x128_f8f6f4 v[158:161], v[2:9], v[190:197], v[158:161], v188, v189 op_sel_hi:[0,0,0]
	v_mfma_scale_f32_16x16x128_f8f6f4 v[154:157], v[10:17], v[190:197], v[154:157], v188, v189 op_sel_hi:[0,0,0]
	v_mfma_scale_f32_16x16x128_f8f6f4 v[150:153], v[2:9], v[198:205], v[150:153], v188, v189 op_sel_hi:[0,0,0]
	v_mfma_scale_f32_16x16x128_f8f6f4 v[146:149], v[10:17], v[198:205], v[146:149], v188, v189 op_sel_hi:[0,0,0]
	v_mfma_scale_f32_16x16x128_f8f6f4 v[138:141], v[2:9], v[206:213], v[138:141], v188, v189 op_sel_hi:[0,0,0]
	v_mfma_scale_f32_16x16x128_f8f6f4 v[130:133], v[10:17], v[206:213], v[130:133], v188, v189 op_sel_hi:[0,0,0]
	v_mfma_scale_f32_16x16x128_f8f6f4 v[122:125], v[2:9], v[220:227], v[122:125], v188, v189 op_sel_hi:[0,0,0]
	v_mfma_scale_f32_16x16x128_f8f6f4 v[114:117], v[10:17], v[220:227], v[114:117], v188, v189 op_sel_hi:[0,0,0]
	v_mfma_scale_f32_16x16x128_f8f6f4 v[142:145], v[18:25], v[190:197], v[142:145], v188, v189 op_sel_hi:[0,0,0]
	v_mfma_scale_f32_16x16x128_f8f6f4 v[134:137], v[26:33], v[190:197], v[134:137], v188, v189 op_sel_hi:[0,0,0]
	v_mfma_scale_f32_16x16x128_f8f6f4 v[126:129], v[18:25], v[198:205], v[126:129], v188, v189 op_sel_hi:[0,0,0]
	v_mfma_scale_f32_16x16x128_f8f6f4 v[118:121], v[26:33], v[198:205], v[118:121], v188, v189 op_sel_hi:[0,0,0]
	v_mfma_scale_f32_16x16x128_f8f6f4 v[110:113], v[18:25], v[206:213], v[110:113], v188, v189 op_sel_hi:[0,0,0]
	v_mfma_scale_f32_16x16x128_f8f6f4 v[106:109], v[26:33], v[206:213], v[106:109], v188, v189 op_sel_hi:[0,0,0]
	v_mfma_scale_f32_16x16x128_f8f6f4 v[102:105], v[18:25], v[220:227], v[102:105], v188, v189 op_sel_hi:[0,0,0]
	v_mfma_scale_f32_16x16x128_f8f6f4 v[98:101], v[26:33], v[220:227], v[98:101], v188, v189 op_sel_hi:[0,0,0]
	s_barrier
	s_add_i32 s26, s54, s57
	v_lshl_add_u64 v[214:215], v[176:177], 0, s[16:17]
	s_mov_b32 m0, s26
	ds_read_b128 v[190:193], v187 offset:49152
	ds_read_b128 v[194:197], v187 offset:50176
	ds_read_b128 v[198:201], v187 offset:51200
	ds_read_b128 v[202:205], v187 offset:52224
	ds_read_b128 v[206:209], v187 offset:53248
	ds_read_b128 v[210:213], v187 offset:54272
	ds_read_b128 v[220:223], v187 offset:55296
	ds_read_b128 v[224:227], v187 offset:56320
	global_load_lds_dwordx4 v[214:215], off
	v_lshl_add_u64 v[214:215], v[176:177], 0, s[18:19]
	s_add_i32 m0, s26, 0x2000
	s_add_i32 s26, s55, s57
	global_load_lds_dwordx4 v[214:215], off
	v_lshl_add_u64 v[214:215], v[176:177], 0, s[22:23]
	s_mov_b32 m0, s26
	v_lshl_add_u64 v[176:177], v[176:177], 0, s[24:25]
	global_load_lds_dwordx4 v[214:215], off
	s_add_i32 m0, s26, 0x2000
	s_nop 0
	global_load_lds_dwordx4 v[176:177], off
	v_lshl_add_u64 v[176:177], v[178:179], 0, s[20:21]
	s_mov_b32 m0, s64
	s_nop 0
	global_load_lds_dwordx4 v[176:177], off
	v_lshl_add_u64 v[176:177], v[180:181], 0, s[20:21]
	s_mov_b32 m0, s65
	s_nop 0
	global_load_lds_dwordx4 v[176:177], off
	s_waitcnt vmcnt(8)
	s_waitcnt lgkmcnt(0)
	s_barrier
	s_waitcnt lgkmcnt(0)
	v_mfma_scale_f32_16x16x128_f8f6f4 v[94:97], v[2:9], v[190:197], v[94:97], v188, v189 op_sel_hi:[0,0,0]
	v_mfma_scale_f32_16x16x128_f8f6f4 v[90:93], v[10:17], v[190:197], v[90:93], v188, v189 op_sel_hi:[0,0,0]
	v_mfma_scale_f32_16x16x128_f8f6f4 v[86:89], v[2:9], v[198:205], v[86:89], v188, v189 op_sel_hi:[0,0,0]
	v_mfma_scale_f32_16x16x128_f8f6f4 v[78:81], v[10:17], v[198:205], v[78:81], v188, v189 op_sel_hi:[0,0,0]
	v_mfma_scale_f32_16x16x128_f8f6f4 v[70:73], v[2:9], v[206:213], v[70:73], v188, v189 op_sel_hi:[0,0,0]
	v_mfma_scale_f32_16x16x128_f8f6f4 v[62:65], v[10:17], v[206:213], v[62:65], v188, v189 op_sel_hi:[0,0,0]
	v_mfma_scale_f32_16x16x128_f8f6f4 v[54:57], v[2:9], v[220:227], v[54:57], v188, v189 op_sel_hi:[0,0,0]
	v_mfma_scale_f32_16x16x128_f8f6f4 v[46:49], v[10:17], v[220:227], v[46:49], v188, v189 op_sel_hi:[0,0,0]
	v_mfma_scale_f32_16x16x128_f8f6f4 v[82:85], v[18:25], v[190:197], v[82:85], v188, v189 op_sel_hi:[0,0,0]
	v_mfma_scale_f32_16x16x128_f8f6f4 v[74:77], v[26:33], v[190:197], v[74:77], v188, v189 op_sel_hi:[0,0,0]
	v_mfma_scale_f32_16x16x128_f8f6f4 v[66:69], v[18:25], v[198:205], v[66:69], v188, v189 op_sel_hi:[0,0,0]
	v_mfma_scale_f32_16x16x128_f8f6f4 v[58:61], v[26:33], v[198:205], v[58:61], v188, v189 op_sel_hi:[0,0,0]
	v_mfma_scale_f32_16x16x128_f8f6f4 v[50:53], v[18:25], v[206:213], v[50:53], v188, v189 op_sel_hi:[0,0,0]
	v_mfma_scale_f32_16x16x128_f8f6f4 v[42:45], v[26:33], v[206:213], v[42:45], v188, v189 op_sel_hi:[0,0,0]
	v_mfma_scale_f32_16x16x128_f8f6f4 v[38:41], v[18:25], v[220:227], v[38:41], v188, v189 op_sel_hi:[0,0,0]
	v_mfma_scale_f32_16x16x128_f8f6f4 v[34:37], v[26:33], v[220:227], v[34:37], v188, v189 op_sel_hi:[0,0,0]
	s_barrier
	s_add_i32 s74, s74, 2
	s_add_u32 s72, s72, 0x10000
	s_addc_u32 s73, s73, 0
	s_add_u32 s50, s50, 0x100
	s_addc_u32 s51, s51, 0
	s_cmp_gt_u32 s74, 41
	s_cbranch_scc0 .LBB0_858
	s_and_b64 vcc, exec, s[40:41]
	s_cbranch_vccz .LBB0_861
	s_barrier

.LBB0_985:
	ds_read_b128 v[26:29], v185
	ds_read_b128 v[30:33], v185 offset:1024
	ds_read_b128 v[18:21], v185 offset:2048
	ds_read_b128 v[22:25], v185 offset:3072
	ds_read_b128 v[10:13], v186
	ds_read_b128 v[14:17], v186 offset:1024
	ds_read_b128 v[2:5], v186 offset:2048
	ds_read_b128 v[6:9], v186 offset:3072
	s_add_u32 s26, s56, 0xfffc0080
	s_addc_u32 s27, s57, -1
	s_cmp_eq_u32 s80, 12
	s_cselect_b32 s59, s45, s27
	s_cselect_b32 s58, s72, s26
	s_cselect_b32 s61, s41, s75
	s_cselect_b32 s60, s73, s74
	v_lshl_add_u64 v[176:177], s[56:57], 0, v[168:169]
	s_add_i32 m0, s55, 0xc000
	ds_read_b128 v[192:195], v187
	ds_read_b128 v[196:199], v187 offset:1024
	ds_read_b128 v[200:203], v187 offset:2048
	ds_read_b128 v[204:207], v187 offset:3072
	ds_read_b128 v[208:211], v187 offset:4096
	ds_read_b128 v[212:215], v187 offset:5120
	ds_read_b128 v[220:223], v187 offset:6144
	ds_read_b128 v[224:227], v187 offset:7168
	global_load_lds_dwordx4 v[176:177], off
	v_lshl_add_u64 v[176:177], s[56:57], 0, v[170:171]
	s_add_i32 m0, s55, 0xe000
	s_nop 0
	global_load_lds_dwordx4 v[176:177], off
	s_waitcnt vmcnt(8)
	s_waitcnt lgkmcnt(0)
	s_barrier
	s_waitcnt lgkmcnt(0)
	v_mfma_scale_f32_16x16x128_f8f6f4 v[158:161], v[26:33], v[192:199], v[158:161], v188, v189 op_sel_hi:[0,0,0]
	v_mfma_scale_f32_16x16x128_f8f6f4 v[154:157], v[18:25], v[192:199], v[154:157], v188, v189 op_sel_hi:[0,0,0]
	v_mfma_scale_f32_16x16x128_f8f6f4 v[146:149], v[26:33], v[200:207], v[146:149], v188, v189 op_sel_hi:[0,0,0]
	v_mfma_scale_f32_16x16x128_f8f6f4 v[138:141], v[18:25], v[200:207], v[138:141], v188, v189 op_sel_hi:[0,0,0]
	v_mfma_scale_f32_16x16x128_f8f6f4 v[130:133], v[26:33], v[208:215], v[130:133], v188, v189 op_sel_hi:[0,0,0]
	v_mfma_scale_f32_16x16x128_f8f6f4 v[122:125], v[18:25], v[208:215], v[122:125], v188, v189 op_sel_hi:[0,0,0]
	v_mfma_scale_f32_16x16x128_f8f6f4 v[114:117], v[26:33], v[220:227], v[114:117], v188, v189 op_sel_hi:[0,0,0]
	v_mfma_scale_f32_16x16x128_f8f6f4 v[106:109], v[18:25], v[220:227], v[106:109], v188, v189 op_sel_hi:[0,0,0]
	v_mfma_scale_f32_16x16x128_f8f6f4 v[150:153], v[10:17], v[192:199], v[150:153], v188, v189 op_sel_hi:[0,0,0]
	v_mfma_scale_f32_16x16x128_f8f6f4 v[142:145], v[2:9], v[192:199], v[142:145], v188, v189 op_sel_hi:[0,0,0]
	v_mfma_scale_f32_16x16x128_f8f6f4 v[134:137], v[10:17], v[200:207], v[134:137], v188, v189 op_sel_hi:[0,0,0]
	v_mfma_scale_f32_16x16x128_f8f6f4 v[126:129], v[2:9], v[200:207], v[126:129], v188, v189 op_sel_hi:[0,0,0]
	v_mfma_scale_f32_16x16x128_f8f6f4 v[118:121], v[10:17], v[208:215], v[118:121], v188, v189 op_sel_hi:[0,0,0]
	v_mfma_scale_f32_16x16x128_f8f6f4 v[110:113], v[2:9], v[208:215], v[110:113], v188, v189 op_sel_hi:[0,0,0]
	v_mfma_scale_f32_16x16x128_f8f6f4 v[102:105], v[10:17], v[220:227], v[102:105], v188, v189 op_sel_hi:[0,0,0]
	v_mfma_scale_f32_16x16x128_f8f6f4 v[98:101], v[2:9], v[220:227], v[98:101], v188, v189 op_sel_hi:[0,0,0]
	s_barrier
	s_add_i32 s26, s70, s35
	v_lshl_add_u64 v[176:177], s[60:61], 0, v[162:163]
	s_mov_b32 m0, s26
	ds_read_b128 v[192:195], v187 offset:16384
	ds_read_b128 v[196:199], v187 offset:17408
	ds_read_b128 v[200:203], v187 offset:18432
	ds_read_b128 v[204:207], v187 offset:19456
	ds_read_b128 v[208:211], v187 offset:20480
	ds_read_b128 v[212:215], v187 offset:21504
	ds_read_b128 v[220:223], v187 offset:22528
	ds_read_b128 v[224:227], v187 offset:23552
	global_load_lds_dwordx4 v[176:177], off
	v_lshl_add_u64 v[178:179], v[176:177], 0, s[6:7]
	s_add_i32 m0, s26, 0x2000
	s_add_i32 s26, s71, s35
	global_load_lds_dwordx4 v[178:179], off
	v_lshl_add_u64 v[178:179], v[176:177], 0, s[8:9]
	s_mov_b32 m0, s26
	v_lshl_add_u64 v[180:181], s[58:59], 0, v[166:167]
	global_load_lds_dwordx4 v[178:179], off
	v_lshl_add_u64 v[178:179], v[176:177], 0, s[10:11]
	s_add_i32 m0, s26, 0x2000
	s_nop 0
	global_load_lds_dwordx4 v[178:179], off
	v_lshl_add_u64 v[178:179], s[58:59], 0, v[164:165]
	s_mov_b32 m0, s55
	s_nop 0
	global_load_lds_dwordx4 v[178:179], off
	s_mov_b32 m0, s63
	s_nop 0
	global_load_lds_dwordx4 v[180:181], off
	s_waitcnt vmcnt(8)
	s_waitcnt lgkmcnt(0)
	s_barrier
	s_waitcnt lgkmcnt(0)
	v_mfma_scale_f32_16x16x128_f8f6f4 v[94:97], v[26:33], v[192:199], v[94:97], v188, v189 op_sel_hi:[0,0,0]
	v_mfma_scale_f32_16x16x128_f8f6f4 v[90:93], v[18:25], v[192:199], v[90:93], v188, v189 op_sel_hi:[0,0,0]
	v_mfma_scale_f32_16x16x128_f8f6f4 v[82:85], v[26:33], v[200:207], v[82:85], v188, v189 op_sel_hi:[0,0,0]
	v_mfma_scale_f32_16x16x128_f8f6f4 v[74:77], v[18:25], v[200:207], v[74:77], v188, v189 op_sel_hi:[0,0,0]
	v_mfma_scale_f32_16x16x128_f8f6f4 v[66:69], v[26:33], v[208:215], v[66:69], v188, v189 op_sel_hi:[0,0,0]
	v_mfma_scale_f32_16x16x128_f8f6f4 v[58:61], v[18:25], v[208:215], v[58:61], v188, v189 op_sel_hi:[0,0,0]
	v_mfma_scale_f32_16x16x128_f8f6f4 v[50:53], v[26:33], v[220:227], v[50:53], v188, v189 op_sel_hi:[0,0,0]
	v_mfma_scale_f32_16x16x128_f8f6f4 v[42:45], v[18:25], v[220:227], v[42:45], v188, v189 op_sel_hi:[0,0,0]
	v_mfma_scale_f32_16x16x128_f8f6f4 v[86:89], v[10:17], v[192:199], v[86:89], v188, v189 op_sel_hi:[0,0,0]
	v_mfma_scale_f32_16x16x128_f8f6f4 v[78:81], v[2:9], v[192:199], v[78:81], v188, v189 op_sel_hi:[0,0,0]
	v_mfma_scale_f32_16x16x128_f8f6f4 v[70:73], v[10:17], v[200:207], v[70:73], v188, v189 op_sel_hi:[0,0,0]
	v_mfma_scale_f32_16x16x128_f8f6f4 v[62:65], v[2:9], v[200:207], v[62:65], v188, v189 op_sel_hi:[0,0,0]
	v_mfma_scale_f32_16x16x128_f8f6f4 v[54:57], v[10:17], v[208:215], v[54:57], v188, v189 op_sel_hi:[0,0,0]
	v_mfma_scale_f32_16x16x128_f8f6f4 v[46:49], v[2:9], v[208:215], v[46:49], v188, v189 op_sel_hi:[0,0,0]
	v_mfma_scale_f32_16x16x128_f8f6f4 v[38:41], v[10:17], v[220:227], v[38:41], v188, v189 op_sel_hi:[0,0,0]
	v_mfma_scale_f32_16x16x128_f8f6f4 v[34:37], v[2:9], v[220:227], v[34:37], v188, v189 op_sel_hi:[0,0,0]
	s_barrier
	s_add_i32 s60, 0, 0x18000
	s_add_i32 s61, 0, 0x1c000
	v_add_u32_e32 v14, s60, v183
	v_add_u32_e32 v30, s61, v183
	ds_read_b128 v[2:5], v14
	ds_read_b128 v[6:9], v14 offset:1024
	ds_read_b128 v[10:13], v14 offset:2048
	ds_read_b128 v[14:17], v14 offset:3072
	ds_read_b128 v[18:21], v30
	ds_read_b128 v[22:25], v30 offset:1024
	ds_read_b128 v[26:29], v30 offset:2048
	ds_read_b128 v[30:33], v30 offset:3072
	s_add_u32 s26, s58, 0x40000
	s_addc_u32 s27, s59, 0
	s_mov_b32 m0, s64
	v_lshl_add_u64 v[216:217], s[26:27], 0, v[164:165]
	ds_read_b128 v[192:195], v187 offset:32768
	ds_read_b128 v[196:199], v187 offset:33792
	ds_read_b128 v[200:203], v187 offset:34816
	ds_read_b128 v[204:207], v187 offset:35840
	ds_read_b128 v[208:211], v187 offset:36864
	ds_read_b128 v[212:215], v187 offset:37888
	ds_read_b128 v[220:223], v187 offset:38912
	ds_read_b128 v[224:227], v187 offset:39936
	global_load_lds_dwordx4 v[216:217], off
	v_lshl_add_u64 v[216:217], s[26:27], 0, v[166:167]
	s_mov_b32 m0, s65
	s_nop 0
	global_load_lds_dwordx4 v[216:217], off
	s_waitcnt vmcnt(8)
	s_waitcnt lgkmcnt(0)
	s_barrier
	s_waitcnt lgkmcnt(0)
	v_mfma_scale_f32_16x16x128_f8f6f4 v[158:161], v[2:9], v[192:199], v[158:161], v188, v189 op_sel_hi:[0,0,0]
	v_mfma_scale_f32_16x16x128_f8f6f4 v[154:157], v[10:17], v[192:199], v[154:157], v188, v189 op_sel_hi:[0,0,0]
	v_mfma_scale_f32_16x16x128_f8f6f4 v[146:149], v[2:9], v[200:207], v[146:149], v188, v189 op_sel_hi:[0,0,0]
	v_mfma_scale_f32_16x16x128_f8f6f4 v[138:141], v[10:17], v[200:207], v[138:141], v188, v189 op_sel_hi:[0,0,0]
	v_mfma_scale_f32_16x16x128_f8f6f4 v[130:133], v[2:9], v[208:215], v[130:133], v188, v189 op_sel_hi:[0,0,0]
	v_mfma_scale_f32_16x16x128_f8f6f4 v[122:125], v[10:17], v[208:215], v[122:125], v188, v189 op_sel_hi:[0,0,0]
	v_mfma_scale_f32_16x16x128_f8f6f4 v[114:117], v[2:9], v[220:227], v[114:117], v188, v189 op_sel_hi:[0,0,0]
	v_mfma_scale_f32_16x16x128_f8f6f4 v[106:109], v[10:17], v[220:227], v[106:109], v188, v189 op_sel_hi:[0,0,0]
	v_mfma_scale_f32_16x16x128_f8f6f4 v[150:153], v[18:25], v[192:199], v[150:153], v188, v189 op_sel_hi:[0,0,0]
	v_mfma_scale_f32_16x16x128_f8f6f4 v[142:145], v[26:33], v[192:199], v[142:145], v188, v189 op_sel_hi:[0,0,0]
	v_mfma_scale_f32_16x16x128_f8f6f4 v[134:137], v[18:25], v[200:207], v[134:137], v188, v189 op_sel_hi:[0,0,0]
	v_mfma_scale_f32_16x16x128_f8f6f4 v[126:129], v[26:33], v[200:207], v[126:129], v188, v189 op_sel_hi:[0,0,0]
	v_mfma_scale_f32_16x16x128_f8f6f4 v[118:121], v[18:25], v[208:215], v[118:121], v188, v189 op_sel_hi:[0,0,0]
	v_mfma_scale_f32_16x16x128_f8f6f4 v[110:113], v[26:33], v[208:215], v[110:113], v188, v189 op_sel_hi:[0,0,0]
	v_mfma_scale_f32_16x16x128_f8f6f4 v[102:105], v[18:25], v[220:227], v[102:105], v188, v189 op_sel_hi:[0,0,0]
	v_mfma_scale_f32_16x16x128_f8f6f4 v[98:101], v[26:33], v[220:227], v[98:101], v188, v189 op_sel_hi:[0,0,0]
	s_barrier
	s_add_i32 s26, s60, s35
	v_lshl_add_u64 v[216:217], v[176:177], 0, s[14:15]
	s_mov_b32 m0, s26
	ds_read_b128 v[192:195], v187 offset:49152
	ds_read_b128 v[196:199], v187 offset:50176
	ds_read_b128 v[200:203], v187 offset:51200
	ds_read_b128 v[204:207], v187 offset:52224
	ds_read_b128 v[208:211], v187 offset:53248
	ds_read_b128 v[212:215], v187 offset:54272
	ds_read_b128 v[220:223], v187 offset:55296
	ds_read_b128 v[224:227], v187 offset:56320
	global_load_lds_dwordx4 v[216:217], off
	v_lshl_add_u64 v[216:217], v[176:177], 0, s[16:17]
	s_add_i32 m0, s26, 0x2000
	s_add_i32 s26, s61, s35
	global_load_lds_dwordx4 v[216:217], off
	v_lshl_add_u64 v[216:217], v[176:177], 0, s[20:21]
	s_mov_b32 m0, s26
	v_lshl_add_u64 v[176:177], v[176:177], 0, s[22:23]
	global_load_lds_dwordx4 v[216:217], off
	s_add_i32 m0, s26, 0x2000
	s_nop 0
	global_load_lds_dwordx4 v[176:177], off
	v_lshl_add_u64 v[176:177], v[178:179], 0, s[18:19]
	s_mov_b32 m0, s67
	s_nop 0
	global_load_lds_dwordx4 v[176:177], off
	v_lshl_add_u64 v[176:177], v[180:181], 0, s[18:19]
	s_mov_b32 m0, s68
	s_nop 0
	global_load_lds_dwordx4 v[176:177], off
	s_waitcnt vmcnt(8)
	s_waitcnt lgkmcnt(0)
	s_barrier
	s_waitcnt lgkmcnt(0)
	v_mfma_scale_f32_16x16x128_f8f6f4 v[94:97], v[2:9], v[192:199], v[94:97], v188, v189 op_sel_hi:[0,0,0]
	v_mfma_scale_f32_16x16x128_f8f6f4 v[90:93], v[10:17], v[192:199], v[90:93], v188, v189 op_sel_hi:[0,0,0]
	v_mfma_scale_f32_16x16x128_f8f6f4 v[82:85], v[2:9], v[200:207], v[82:85], v188, v189 op_sel_hi:[0,0,0]
	v_mfma_scale_f32_16x16x128_f8f6f4 v[74:77], v[10:17], v[200:207], v[74:77], v188, v189 op_sel_hi:[0,0,0]
	v_mfma_scale_f32_16x16x128_f8f6f4 v[66:69], v[2:9], v[208:215], v[66:69], v188, v189 op_sel_hi:[0,0,0]
	v_mfma_scale_f32_16x16x128_f8f6f4 v[58:61], v[10:17], v[208:215], v[58:61], v188, v189 op_sel_hi:[0,0,0]
	v_mfma_scale_f32_16x16x128_f8f6f4 v[50:53], v[2:9], v[220:227], v[50:53], v188, v189 op_sel_hi:[0,0,0]
	v_mfma_scale_f32_16x16x128_f8f6f4 v[42:45], v[10:17], v[220:227], v[42:45], v188, v189 op_sel_hi:[0,0,0]
	v_mfma_scale_f32_16x16x128_f8f6f4 v[86:89], v[18:25], v[192:199], v[86:89], v188, v189 op_sel_hi:[0,0,0]
	v_mfma_scale_f32_16x16x128_f8f6f4 v[78:81], v[26:33], v[192:199], v[78:81], v188, v189 op_sel_hi:[0,0,0]
	v_mfma_scale_f32_16x16x128_f8f6f4 v[70:73], v[18:25], v[200:207], v[70:73], v188, v189 op_sel_hi:[0,0,0]
	v_mfma_scale_f32_16x16x128_f8f6f4 v[62:65], v[26:33], v[200:207], v[62:65], v188, v189 op_sel_hi:[0,0,0]
	v_mfma_scale_f32_16x16x128_f8f6f4 v[54:57], v[18:25], v[208:215], v[54:57], v188, v189 op_sel_hi:[0,0,0]
	v_mfma_scale_f32_16x16x128_f8f6f4 v[46:49], v[26:33], v[208:215], v[46:49], v188, v189 op_sel_hi:[0,0,0]
	v_mfma_scale_f32_16x16x128_f8f6f4 v[38:41], v[18:25], v[220:227], v[38:41], v188, v189 op_sel_hi:[0,0,0]
	v_mfma_scale_f32_16x16x128_f8f6f4 v[34:37], v[26:33], v[220:227], v[34:37], v188, v189 op_sel_hi:[0,0,0]
	s_barrier
	s_add_i32 s80, s80, 2
	s_add_u32 s74, s74, 0x10000
	s_addc_u32 s75, s75, 0
	s_add_u32 s56, s56, 0x100
	s_addc_u32 s57, s57, 0
	s_cmp_gt_u32 s80, 13
	s_cbranch_scc0 .LBB0_985
	s_and_b64 vcc, exec, s[24:25]
	s_cbranch_vccz .LBB0_988
	s_barrier

.LBB0_1192:
	ds_read_b128 v[66:69], v199
	ds_read_b128 v[70:73], v199 offset:1024
	ds_read_b128 v[82:85], v199 offset:2048
	ds_read_b128 v[86:89], v199 offset:3072
	ds_read_b128 v[146:149], v200
	ds_read_b128 v[150:153], v200 offset:1024
	ds_read_b128 v[154:157], v200 offset:2048
	ds_read_b128 v[158:161], v200 offset:3072
	s_add_u32 s26, s56, 0xfffc0080
	s_addc_u32 s27, s57, -1
	s_cmp_eq_u32 s73, 12
	s_cselect_b32 s59, s45, s27
	s_cselect_b32 s58, s69, s26
	s_cselect_b32 s27, s41, s72
	s_cselect_b32 s26, s70, s71
	v_lshl_add_u64 v[214:215], s[56:57], 0, v[176:177]
	s_add_i32 m0, s55, 0xc000
	ds_read_b128 v[162:165], v201
	ds_read_b128 v[166:169], v201 offset:1024
	ds_read_b128 v[184:187], v201 offset:2048
	ds_read_b128 v[188:191], v201 offset:3072
	ds_read_b128 v[192:195], v201 offset:4096
	ds_read_b128 v[202:205], v201 offset:5120
	ds_read_b128 v[206:209], v201 offset:6144
	ds_read_b128 v[210:213], v201 offset:7168
	global_load_lds_dwordx4 v[214:215], off
	v_lshl_add_u64 v[214:215], s[56:57], 0, v[178:179]
	s_add_i32 m0, s55, 0xe000
	s_nop 0
	global_load_lds_dwordx4 v[214:215], off
	s_waitcnt vmcnt(8)
	s_waitcnt lgkmcnt(0)
	s_barrier
	s_waitcnt lgkmcnt(0)
	v_mfma_f32_16x16x32_bf16 v[142:145], v[66:69], v[162:165], v[142:145]
	v_mfma_f32_16x16x32_bf16 v[138:141], v[82:85], v[162:165], v[138:141]
	v_mfma_f32_16x16x32_bf16 v[126:129], v[66:69], v[184:187], v[126:129]
	v_mfma_f32_16x16x32_bf16 v[122:125], v[82:85], v[184:187], v[122:125]
	v_mfma_f32_16x16x32_bf16 v[110:113], v[66:69], v[192:195], v[110:113]
	v_mfma_f32_16x16x32_bf16 v[106:109], v[82:85], v[192:195], v[106:109]
	v_mfma_f32_16x16x32_bf16 v[94:97], v[66:69], v[206:209], v[94:97]
	v_mfma_f32_16x16x32_bf16 v[90:93], v[82:85], v[206:209], v[90:93]
	v_mfma_f32_16x16x32_bf16 v[142:145], v[70:73], v[166:169], v[142:145]
	v_mfma_f32_16x16x32_bf16 v[138:141], v[86:89], v[166:169], v[138:141]
	v_mfma_f32_16x16x32_bf16 v[126:129], v[70:73], v[188:191], v[126:129]
	v_mfma_f32_16x16x32_bf16 v[122:125], v[86:89], v[188:191], v[122:125]
	v_mfma_f32_16x16x32_bf16 v[110:113], v[70:73], v[202:205], v[110:113]
	v_mfma_f32_16x16x32_bf16 v[106:109], v[86:89], v[202:205], v[106:109]
	v_mfma_f32_16x16x32_bf16 v[94:97], v[70:73], v[210:213], v[94:97]
	v_mfma_f32_16x16x32_bf16 v[90:93], v[86:89], v[210:213], v[90:93]
	v_mfma_f32_16x16x32_bf16 v[134:137], v[146:149], v[162:165], v[134:137]
	v_mfma_f32_16x16x32_bf16 v[130:133], v[154:157], v[162:165], v[130:133]
	v_mfma_f32_16x16x32_bf16 v[118:121], v[146:149], v[184:187], v[118:121]
	v_mfma_f32_16x16x32_bf16 v[114:117], v[154:157], v[184:187], v[114:117]
	v_mfma_f32_16x16x32_bf16 v[102:105], v[146:149], v[192:195], v[102:105]
	v_mfma_f32_16x16x32_bf16 v[98:101], v[154:157], v[192:195], v[98:101]
	v_mfma_f32_16x16x32_bf16 v[78:81], v[146:149], v[206:209], v[78:81]
	v_mfma_f32_16x16x32_bf16 v[74:77], v[154:157], v[206:209], v[74:77]
	v_mfma_f32_16x16x32_bf16 v[134:137], v[150:153], v[166:169], v[134:137]
	v_mfma_f32_16x16x32_bf16 v[130:133], v[158:161], v[166:169], v[130:133]
	v_mfma_f32_16x16x32_bf16 v[118:121], v[150:153], v[188:191], v[118:121]
	v_mfma_f32_16x16x32_bf16 v[114:117], v[158:161], v[188:191], v[114:117]
	v_mfma_f32_16x16x32_bf16 v[102:105], v[150:153], v[202:205], v[102:105]
	v_mfma_f32_16x16x32_bf16 v[98:101], v[158:161], v[202:205], v[98:101]
	v_mfma_f32_16x16x32_bf16 v[78:81], v[150:153], v[210:213], v[78:81]
	v_mfma_f32_16x16x32_bf16 v[74:77], v[158:161], v[210:213], v[74:77]
	s_barrier
	v_lshl_add_u64 v[214:215], s[26:27], 0, v[170:171]
	s_add_i32 s26, s67, s35
	s_mov_b32 m0, s26
	ds_read_b128 v[162:165], v201 offset:16384
	ds_read_b128 v[166:169], v201 offset:17408
	ds_read_b128 v[184:187], v201 offset:18432
	ds_read_b128 v[188:191], v201 offset:19456
	ds_read_b128 v[192:195], v201 offset:20480
	ds_read_b128 v[202:205], v201 offset:21504
	ds_read_b128 v[206:209], v201 offset:22528
	ds_read_b128 v[210:213], v201 offset:23552
	global_load_lds_dwordx4 v[214:215], off
	v_lshl_add_u64 v[216:217], v[214:215], 0, s[6:7]
	s_add_i32 m0, s26, 0x2000
	s_add_i32 s26, s68, s35
	global_load_lds_dwordx4 v[216:217], off
	v_lshl_add_u64 v[216:217], v[214:215], 0, s[10:11]
	s_mov_b32 m0, s26
	v_lshl_add_u64 v[220:221], s[58:59], 0, v[174:175]
	global_load_lds_dwordx4 v[216:217], off
	v_lshl_add_u64 v[216:217], v[214:215], 0, s[12:13]
	s_add_i32 m0, s26, 0x2000
	s_nop 0
	global_load_lds_dwordx4 v[216:217], off
	v_lshl_add_u64 v[216:217], s[58:59], 0, v[172:173]
	s_mov_b32 m0, s55
	s_nop 0
	global_load_lds_dwordx4 v[216:217], off
	s_mov_b32 m0, s60
	s_nop 0
	global_load_lds_dwordx4 v[220:221], off
	s_waitcnt vmcnt(8)
	s_waitcnt lgkmcnt(0)
	s_barrier
	s_waitcnt lgkmcnt(0)
	v_mfma_f32_16x16x32_bf16 v[62:65], v[66:69], v[162:165], v[62:65]
	v_mfma_f32_16x16x32_bf16 v[58:61], v[82:85], v[162:165], v[58:61]
	v_mfma_f32_16x16x32_bf16 v[46:49], v[66:69], v[184:187], v[46:49]
	v_mfma_f32_16x16x32_bf16 v[42:45], v[82:85], v[184:187], v[42:45]
	v_mfma_f32_16x16x32_bf16 v[30:33], v[66:69], v[192:195], v[30:33]
	v_mfma_f32_16x16x32_bf16 v[26:29], v[82:85], v[192:195], v[26:29]
	v_mfma_f32_16x16x32_bf16 v[14:17], v[66:69], v[206:209], v[14:17]
	v_mfma_f32_16x16x32_bf16 v[10:13], v[82:85], v[206:209], v[10:13]
	v_mfma_f32_16x16x32_bf16 v[62:65], v[70:73], v[166:169], v[62:65]
	v_mfma_f32_16x16x32_bf16 v[58:61], v[86:89], v[166:169], v[58:61]
	v_mfma_f32_16x16x32_bf16 v[46:49], v[70:73], v[188:191], v[46:49]
	v_mfma_f32_16x16x32_bf16 v[42:45], v[86:89], v[188:191], v[42:45]
	v_mfma_f32_16x16x32_bf16 v[30:33], v[70:73], v[202:205], v[30:33]
	v_mfma_f32_16x16x32_bf16 v[26:29], v[86:89], v[202:205], v[26:29]
	v_mfma_f32_16x16x32_bf16 v[14:17], v[70:73], v[210:213], v[14:17]
	v_mfma_f32_16x16x32_bf16 v[10:13], v[86:89], v[210:213], v[10:13]
	v_mfma_f32_16x16x32_bf16 v[54:57], v[146:149], v[162:165], v[54:57]
	v_mfma_f32_16x16x32_bf16 v[50:53], v[154:157], v[162:165], v[50:53]
	v_mfma_f32_16x16x32_bf16 v[38:41], v[146:149], v[184:187], v[38:41]
	v_mfma_f32_16x16x32_bf16 v[34:37], v[154:157], v[184:187], v[34:37]
	v_mfma_f32_16x16x32_bf16 v[22:25], v[146:149], v[192:195], v[22:25]
	v_mfma_f32_16x16x32_bf16 v[18:21], v[154:157], v[192:195], v[18:21]
	v_mfma_f32_16x16x32_bf16 v[6:9], v[146:149], v[206:209], v[6:9]
	v_mfma_f32_16x16x32_bf16 v[2:5], v[154:157], v[206:209], v[2:5]
	v_mfma_f32_16x16x32_bf16 v[54:57], v[150:153], v[166:169], v[54:57]
	v_mfma_f32_16x16x32_bf16 v[50:53], v[158:161], v[166:169], v[50:53]
	v_mfma_f32_16x16x32_bf16 v[38:41], v[150:153], v[188:191], v[38:41]
	v_mfma_f32_16x16x32_bf16 v[34:37], v[158:161], v[188:191], v[34:37]
	v_mfma_f32_16x16x32_bf16 v[22:25], v[150:153], v[202:205], v[22:25]
	v_mfma_f32_16x16x32_bf16 v[18:21], v[158:161], v[202:205], v[18:21]
	v_mfma_f32_16x16x32_bf16 v[6:9], v[150:153], v[210:213], v[6:9]
	v_mfma_f32_16x16x32_bf16 v[2:5], v[158:161], v[210:213], v[2:5]
	s_barrier
	s_add_i32 s74, 0, 0x18000
	s_add_i32 s75, 0, 0x1c000
	v_add_u32_e32 v86, s74, v197
	v_add_u32_e32 v158, s75, v197
	ds_read_b128 v[66:69], v86
	ds_read_b128 v[70:73], v86 offset:1024
	ds_read_b128 v[82:85], v86 offset:2048
	ds_read_b128 v[86:89], v86 offset:3072
	ds_read_b128 v[146:149], v158
	ds_read_b128 v[150:153], v158 offset:1024
	ds_read_b128 v[154:157], v158 offset:2048
	ds_read_b128 v[158:161], v158 offset:3072
	s_add_u32 s26, s58, 0x40000
	s_addc_u32 s27, s59, 0
	s_mov_b32 m0, s61
	v_lshl_add_u64 v[222:223], s[26:27], 0, v[172:173]
	ds_read_b128 v[162:165], v201 offset:32768
	ds_read_b128 v[166:169], v201 offset:33792
	ds_read_b128 v[184:187], v201 offset:34816
	ds_read_b128 v[188:191], v201 offset:35840
	ds_read_b128 v[192:195], v201 offset:36864
	ds_read_b128 v[202:205], v201 offset:37888
	ds_read_b128 v[206:209], v201 offset:38912
	ds_read_b128 v[210:213], v201 offset:39936
	global_load_lds_dwordx4 v[222:223], off
	v_lshl_add_u64 v[222:223], s[26:27], 0, v[174:175]
	s_mov_b32 m0, s62
	s_nop 0
	global_load_lds_dwordx4 v[222:223], off
	s_waitcnt vmcnt(8)
	s_waitcnt lgkmcnt(0)
	s_barrier
	s_waitcnt lgkmcnt(0)
	v_mfma_f32_16x16x32_bf16 v[142:145], v[66:69], v[162:165], v[142:145]
	v_mfma_f32_16x16x32_bf16 v[138:141], v[82:85], v[162:165], v[138:141]
	v_mfma_f32_16x16x32_bf16 v[126:129], v[66:69], v[184:187], v[126:129]
	v_mfma_f32_16x16x32_bf16 v[122:125], v[82:85], v[184:187], v[122:125]
	v_mfma_f32_16x16x32_bf16 v[110:113], v[66:69], v[192:195], v[110:113]
	v_mfma_f32_16x16x32_bf16 v[106:109], v[82:85], v[192:195], v[106:109]
	v_mfma_f32_16x16x32_bf16 v[94:97], v[66:69], v[206:209], v[94:97]
	v_mfma_f32_16x16x32_bf16 v[90:93], v[82:85], v[206:209], v[90:93]
	v_mfma_f32_16x16x32_bf16 v[142:145], v[70:73], v[166:169], v[142:145]
	v_mfma_f32_16x16x32_bf16 v[138:141], v[86:89], v[166:169], v[138:141]
	v_mfma_f32_16x16x32_bf16 v[126:129], v[70:73], v[188:191], v[126:129]
	v_mfma_f32_16x16x32_bf16 v[122:125], v[86:89], v[188:191], v[122:125]
	v_mfma_f32_16x16x32_bf16 v[110:113], v[70:73], v[202:205], v[110:113]
	v_mfma_f32_16x16x32_bf16 v[106:109], v[86:89], v[202:205], v[106:109]
	v_mfma_f32_16x16x32_bf16 v[94:97], v[70:73], v[210:213], v[94:97]
	v_mfma_f32_16x16x32_bf16 v[90:93], v[86:89], v[210:213], v[90:93]
	v_mfma_f32_16x16x32_bf16 v[134:137], v[146:149], v[162:165], v[134:137]
	v_mfma_f32_16x16x32_bf16 v[130:133], v[154:157], v[162:165], v[130:133]
	v_mfma_f32_16x16x32_bf16 v[118:121], v[146:149], v[184:187], v[118:121]
	v_mfma_f32_16x16x32_bf16 v[114:117], v[154:157], v[184:187], v[114:117]
	v_mfma_f32_16x16x32_bf16 v[102:105], v[146:149], v[192:195], v[102:105]
	v_mfma_f32_16x16x32_bf16 v[98:101], v[154:157], v[192:195], v[98:101]
	v_mfma_f32_16x16x32_bf16 v[78:81], v[146:149], v[206:209], v[78:81]
	v_mfma_f32_16x16x32_bf16 v[74:77], v[154:157], v[206:209], v[74:77]
	v_mfma_f32_16x16x32_bf16 v[134:137], v[150:153], v[166:169], v[134:137]
	v_mfma_f32_16x16x32_bf16 v[130:133], v[158:161], v[166:169], v[130:133]
	v_mfma_f32_16x16x32_bf16 v[118:121], v[150:153], v[188:191], v[118:121]
	v_mfma_f32_16x16x32_bf16 v[114:117], v[158:161], v[188:191], v[114:117]
	v_mfma_f32_16x16x32_bf16 v[102:105], v[150:153], v[202:205], v[102:105]
	v_mfma_f32_16x16x32_bf16 v[98:101], v[158:161], v[202:205], v[98:101]
	v_mfma_f32_16x16x32_bf16 v[78:81], v[150:153], v[210:213], v[78:81]
	v_mfma_f32_16x16x32_bf16 v[74:77], v[158:161], v[210:213], v[74:77]
	s_barrier
	s_add_i32 s26, s74, s35
	v_lshl_add_u64 v[222:223], v[214:215], 0, s[16:17]
	s_mov_b32 m0, s26
	ds_read_b128 v[162:165], v201 offset:49152
	ds_read_b128 v[166:169], v201 offset:50176
	ds_read_b128 v[184:187], v201 offset:51200
	ds_read_b128 v[188:191], v201 offset:52224
	ds_read_b128 v[192:195], v201 offset:53248
	ds_read_b128 v[202:205], v201 offset:54272
	ds_read_b128 v[206:209], v201 offset:55296
	ds_read_b128 v[210:213], v201 offset:56320
	global_load_lds_dwordx4 v[222:223], off
	v_lshl_add_u64 v[222:223], v[214:215], 0, s[18:19]
	s_add_i32 m0, s26, 0x2000
	s_add_i32 s26, s75, s35
	global_load_lds_dwordx4 v[222:223], off
	v_lshl_add_u64 v[222:223], v[214:215], 0, s[22:23]
	s_mov_b32 m0, s26
	v_lshl_add_u64 v[214:215], v[214:215], 0, s[24:25]
	global_load_lds_dwordx4 v[222:223], off
	s_add_i32 m0, s26, 0x2000
	s_nop 0
	global_load_lds_dwordx4 v[214:215], off
	v_lshl_add_u64 v[214:215], v[216:217], 0, s[20:21]
	s_mov_b32 m0, s64
	s_nop 0
	global_load_lds_dwordx4 v[214:215], off
	v_lshl_add_u64 v[214:215], v[220:221], 0, s[20:21]
	s_mov_b32 m0, s65
	s_nop 0
	global_load_lds_dwordx4 v[214:215], off
	s_waitcnt vmcnt(8)
	s_waitcnt lgkmcnt(0)
	s_barrier
	s_waitcnt lgkmcnt(0)
	v_mfma_f32_16x16x32_bf16 v[62:65], v[66:69], v[162:165], v[62:65]
	v_mfma_f32_16x16x32_bf16 v[58:61], v[82:85], v[162:165], v[58:61]
	v_mfma_f32_16x16x32_bf16 v[46:49], v[66:69], v[184:187], v[46:49]
	v_mfma_f32_16x16x32_bf16 v[42:45], v[82:85], v[184:187], v[42:45]
	v_mfma_f32_16x16x32_bf16 v[30:33], v[66:69], v[192:195], v[30:33]
	v_mfma_f32_16x16x32_bf16 v[26:29], v[82:85], v[192:195], v[26:29]
	v_mfma_f32_16x16x32_bf16 v[14:17], v[66:69], v[206:209], v[14:17]
	v_mfma_f32_16x16x32_bf16 v[10:13], v[82:85], v[206:209], v[10:13]
	v_mfma_f32_16x16x32_bf16 v[62:65], v[70:73], v[166:169], v[62:65]
	v_mfma_f32_16x16x32_bf16 v[58:61], v[86:89], v[166:169], v[58:61]
	v_mfma_f32_16x16x32_bf16 v[46:49], v[70:73], v[188:191], v[46:49]
	v_mfma_f32_16x16x32_bf16 v[42:45], v[86:89], v[188:191], v[42:45]
	v_mfma_f32_16x16x32_bf16 v[30:33], v[70:73], v[202:205], v[30:33]
	v_mfma_f32_16x16x32_bf16 v[26:29], v[86:89], v[202:205], v[26:29]
	v_mfma_f32_16x16x32_bf16 v[14:17], v[70:73], v[210:213], v[14:17]
	v_mfma_f32_16x16x32_bf16 v[10:13], v[86:89], v[210:213], v[10:13]
	v_mfma_f32_16x16x32_bf16 v[54:57], v[146:149], v[162:165], v[54:57]
	v_mfma_f32_16x16x32_bf16 v[50:53], v[154:157], v[162:165], v[50:53]
	v_mfma_f32_16x16x32_bf16 v[38:41], v[146:149], v[184:187], v[38:41]
	v_mfma_f32_16x16x32_bf16 v[34:37], v[154:157], v[184:187], v[34:37]
	v_mfma_f32_16x16x32_bf16 v[22:25], v[146:149], v[192:195], v[22:25]
	v_mfma_f32_16x16x32_bf16 v[18:21], v[154:157], v[192:195], v[18:21]
	v_mfma_f32_16x16x32_bf16 v[6:9], v[146:149], v[206:209], v[6:9]
	v_mfma_f32_16x16x32_bf16 v[2:5], v[154:157], v[206:209], v[2:5]
	v_mfma_f32_16x16x32_bf16 v[54:57], v[150:153], v[166:169], v[54:57]
	v_mfma_f32_16x16x32_bf16 v[50:53], v[158:161], v[166:169], v[50:53]
	v_mfma_f32_16x16x32_bf16 v[38:41], v[150:153], v[188:191], v[38:41]
	v_mfma_f32_16x16x32_bf16 v[34:37], v[158:161], v[188:191], v[34:37]
	v_mfma_f32_16x16x32_bf16 v[22:25], v[150:153], v[202:205], v[22:25]
	v_mfma_f32_16x16x32_bf16 v[18:21], v[158:161], v[202:205], v[18:21]
	v_mfma_f32_16x16x32_bf16 v[6:9], v[150:153], v[210:213], v[6:9]
	v_mfma_f32_16x16x32_bf16 v[2:5], v[158:161], v[210:213], v[2:5]
	s_barrier
	s_add_i32 s73, s73, 2
	s_add_u32 s71, s71, 0x10000
	s_addc_u32 s72, s72, 0
	s_add_u32 s56, s56, 0x100
	s_addc_u32 s57, s57, 0
	s_cmp_gt_u32 s73, 13
	s_cbranch_scc0 .LBB0_1192
	s_and_b64 vcc, exec, s[36:37]
	s_cbranch_vccz .LBB0_1195
	s_barrier

.LBB0_1271:
	ds_read_b128 v[144:147], v158
	ds_read_b128 v[148:151], v158 offset:1024
	ds_read_b128 v[152:155], v158 offset:2048
	ds_read_b128 v[162:165], v158 offset:3072
	ds_read_b128 v[166:169], v159
	ds_read_b128 v[170:173], v159 offset:1024
	ds_read_b128 v[174:177], v159 offset:2048
	ds_read_b128 v[178:181], v159 offset:3072
	s_add_u32 s26, s58, 0xfff80080
	s_addc_u32 s27, s59, -1
	s_cmp_eq_u32 s80, 28
	s_cselect_b32 s61, s51, s27
	s_cselect_b32 s60, s57, s26
	s_cselect_b32 s27, s45, s75
	s_cselect_b32 s26, s73, s74
	v_lshl_add_u64 v[214:215], s[58:59], 0, v[136:137]
	s_add_i32 m0, s63, 0xc000
	ds_read_b128 v[182:185], v160
	ds_read_b128 v[186:189], v160 offset:1024
	ds_read_b128 v[190:193], v160 offset:2048
	ds_read_b128 v[194:197], v160 offset:3072
	ds_read_b128 v[198:201], v160 offset:4096
	ds_read_b128 v[202:205], v160 offset:5120
	ds_read_b128 v[206:209], v160 offset:6144
	ds_read_b128 v[210:213], v160 offset:7168
	global_load_lds_dwordx4 v[214:215], off
	v_lshl_add_u64 v[214:215], s[58:59], 0, v[138:139]
	s_add_i32 m0, s63, 0xe000
	s_nop 0
	global_load_lds_dwordx4 v[214:215], off
	s_waitcnt vmcnt(8)
	s_waitcnt lgkmcnt(0)
	s_barrier
	s_waitcnt lgkmcnt(0)
	v_mfma_f32_16x16x32_bf16 v[126:129], v[144:147], v[182:185], v[126:129]
	v_mfma_f32_16x16x32_bf16 v[122:125], v[152:155], v[182:185], v[122:125]
	v_mfma_f32_16x16x32_bf16 v[118:121], v[144:147], v[190:193], v[118:121]
	v_mfma_f32_16x16x32_bf16 v[114:117], v[152:155], v[190:193], v[114:117]
	v_mfma_f32_16x16x32_bf16 v[106:109], v[144:147], v[198:201], v[106:109]
	v_mfma_f32_16x16x32_bf16 v[98:101], v[152:155], v[198:201], v[98:101]
	v_mfma_f32_16x16x32_bf16 v[90:93], v[144:147], v[206:209], v[90:93]
	v_mfma_f32_16x16x32_bf16 v[82:85], v[152:155], v[206:209], v[82:85]
	v_mfma_f32_16x16x32_bf16 v[126:129], v[148:151], v[186:189], v[126:129]
	v_mfma_f32_16x16x32_bf16 v[122:125], v[162:165], v[186:189], v[122:125]
	v_mfma_f32_16x16x32_bf16 v[118:121], v[148:151], v[194:197], v[118:121]
	v_mfma_f32_16x16x32_bf16 v[114:117], v[162:165], v[194:197], v[114:117]
	v_mfma_f32_16x16x32_bf16 v[106:109], v[148:151], v[202:205], v[106:109]
	v_mfma_f32_16x16x32_bf16 v[98:101], v[162:165], v[202:205], v[98:101]
	v_mfma_f32_16x16x32_bf16 v[90:93], v[148:151], v[210:213], v[90:93]
	v_mfma_f32_16x16x32_bf16 v[82:85], v[162:165], v[210:213], v[82:85]
	v_mfma_f32_16x16x32_bf16 v[110:113], v[166:169], v[182:185], v[110:113]
	v_mfma_f32_16x16x32_bf16 v[102:105], v[174:177], v[182:185], v[102:105]
	v_mfma_f32_16x16x32_bf16 v[94:97], v[166:169], v[190:193], v[94:97]
	v_mfma_f32_16x16x32_bf16 v[86:89], v[174:177], v[190:193], v[86:89]
	v_mfma_f32_16x16x32_bf16 v[78:81], v[166:169], v[198:201], v[78:81]
	v_mfma_f32_16x16x32_bf16 v[74:77], v[174:177], v[198:201], v[74:77]
	v_mfma_f32_16x16x32_bf16 v[70:73], v[166:169], v[206:209], v[70:73]
	v_mfma_f32_16x16x32_bf16 v[66:69], v[174:177], v[206:209], v[66:69]
	v_mfma_f32_16x16x32_bf16 v[110:113], v[170:173], v[186:189], v[110:113]
	v_mfma_f32_16x16x32_bf16 v[102:105], v[178:181], v[186:189], v[102:105]
	v_mfma_f32_16x16x32_bf16 v[94:97], v[170:173], v[194:197], v[94:97]
	v_mfma_f32_16x16x32_bf16 v[86:89], v[178:181], v[194:197], v[86:89]
	v_mfma_f32_16x16x32_bf16 v[78:81], v[170:173], v[202:205], v[78:81]
	v_mfma_f32_16x16x32_bf16 v[74:77], v[178:181], v[202:205], v[74:77]
	v_mfma_f32_16x16x32_bf16 v[70:73], v[170:173], v[210:213], v[70:73]
	v_mfma_f32_16x16x32_bf16 v[66:69], v[178:181], v[210:213], v[66:69]
	s_barrier
	v_lshl_add_u64 v[214:215], s[26:27], 0, v[130:131]
	s_add_i32 s26, s71, s35
	s_mov_b32 m0, s26
	ds_read_b128 v[182:185], v160 offset:16384
	ds_read_b128 v[186:189], v160 offset:17408
	ds_read_b128 v[190:193], v160 offset:18432
	ds_read_b128 v[194:197], v160 offset:19456
	ds_read_b128 v[198:201], v160 offset:20480
	ds_read_b128 v[202:205], v160 offset:21504
	ds_read_b128 v[206:209], v160 offset:22528
	ds_read_b128 v[210:213], v160 offset:23552
	global_load_lds_dwordx4 v[214:215], off
	v_lshl_add_u64 v[216:217], v[214:215], 0, s[6:7]
	s_add_i32 m0, s26, 0x2000
	s_add_i32 s26, s72, s35
	global_load_lds_dwordx4 v[216:217], off
	v_lshl_add_u64 v[216:217], v[214:215], 0, s[8:9]
	s_mov_b32 m0, s26
	v_lshl_add_u64 v[220:221], s[60:61], 0, v[134:135]
	global_load_lds_dwordx4 v[216:217], off
	v_lshl_add_u64 v[216:217], v[214:215], 0, s[10:11]
	s_add_i32 m0, s26, 0x2000
	s_nop 0
	global_load_lds_dwordx4 v[216:217], off
	v_lshl_add_u64 v[216:217], s[60:61], 0, v[132:133]
	s_mov_b32 m0, s63
	s_nop 0
	global_load_lds_dwordx4 v[216:217], off
	s_mov_b32 m0, s64
	s_nop 0
	global_load_lds_dwordx4 v[220:221], off
	s_waitcnt vmcnt(8)
	s_waitcnt lgkmcnt(0)
	s_barrier
	s_waitcnt lgkmcnt(0)
	v_mfma_f32_16x16x32_bf16 v[62:65], v[144:147], v[182:185], v[62:65]
	v_mfma_f32_16x16x32_bf16 v[58:61], v[152:155], v[182:185], v[58:61]
	v_mfma_f32_16x16x32_bf16 v[54:57], v[144:147], v[190:193], v[54:57]
	v_mfma_f32_16x16x32_bf16 v[46:49], v[152:155], v[190:193], v[46:49]
	v_mfma_f32_16x16x32_bf16 v[38:41], v[144:147], v[198:201], v[38:41]
	v_mfma_f32_16x16x32_bf16 v[30:33], v[152:155], v[198:201], v[30:33]
	v_mfma_f32_16x16x32_bf16 v[22:25], v[144:147], v[206:209], v[22:25]
	v_mfma_f32_16x16x32_bf16 v[14:17], v[152:155], v[206:209], v[14:17]
	v_mfma_f32_16x16x32_bf16 v[62:65], v[148:151], v[186:189], v[62:65]
	v_mfma_f32_16x16x32_bf16 v[58:61], v[162:165], v[186:189], v[58:61]
	v_mfma_f32_16x16x32_bf16 v[54:57], v[148:151], v[194:197], v[54:57]
	v_mfma_f32_16x16x32_bf16 v[46:49], v[162:165], v[194:197], v[46:49]
	v_mfma_f32_16x16x32_bf16 v[38:41], v[148:151], v[202:205], v[38:41]
	v_mfma_f32_16x16x32_bf16 v[30:33], v[162:165], v[202:205], v[30:33]
	v_mfma_f32_16x16x32_bf16 v[22:25], v[148:151], v[210:213], v[22:25]
	v_mfma_f32_16x16x32_bf16 v[14:17], v[162:165], v[210:213], v[14:17]
	v_mfma_f32_16x16x32_bf16 v[50:53], v[166:169], v[182:185], v[50:53]
	v_mfma_f32_16x16x32_bf16 v[42:45], v[174:177], v[182:185], v[42:45]
	v_mfma_f32_16x16x32_bf16 v[34:37], v[166:169], v[190:193], v[34:37]
	v_mfma_f32_16x16x32_bf16 v[26:29], v[174:177], v[190:193], v[26:29]
	v_mfma_f32_16x16x32_bf16 v[18:21], v[166:169], v[198:201], v[18:21]
	v_mfma_f32_16x16x32_bf16 v[10:13], v[174:177], v[198:201], v[10:13]
	v_mfma_f32_16x16x32_bf16 v[6:9], v[166:169], v[206:209], v[6:9]
	v_mfma_f32_16x16x32_bf16 v[2:5], v[174:177], v[206:209], v[2:5]
	v_mfma_f32_16x16x32_bf16 v[50:53], v[170:173], v[186:189], v[50:53]
	v_mfma_f32_16x16x32_bf16 v[42:45], v[178:181], v[186:189], v[42:45]
	v_mfma_f32_16x16x32_bf16 v[34:37], v[170:173], v[194:197], v[34:37]
	v_mfma_f32_16x16x32_bf16 v[26:29], v[178:181], v[194:197], v[26:29]
	v_mfma_f32_16x16x32_bf16 v[18:21], v[170:173], v[202:205], v[18:21]
	v_mfma_f32_16x16x32_bf16 v[10:13], v[178:181], v[202:205], v[10:13]
	v_mfma_f32_16x16x32_bf16 v[6:9], v[170:173], v[210:213], v[6:9]
	v_mfma_f32_16x16x32_bf16 v[2:5], v[178:181], v[210:213], v[2:5]
	s_barrier
	s_add_i32 s81, 0, 0x18000
	v_add_u32_e32 v161, s81, v156
	s_add_i32 s82, 0, 0x1c000
	ds_read_b128 v[144:147], v161
	ds_read_b128 v[148:151], v161 offset:1024
	ds_read_b128 v[152:155], v161 offset:2048
	ds_read_b128 v[162:165], v161 offset:3072
	v_add_u32_e32 v161, s82, v156
	ds_read_b128 v[166:169], v161
	ds_read_b128 v[170:173], v161 offset:1024
	ds_read_b128 v[174:177], v161 offset:2048
	ds_read_b128 v[178:181], v161 offset:3072
	s_add_u32 s26, s60, 0x80000
	s_addc_u32 s27, s61, 0
	s_mov_b32 m0, s65
	v_lshl_add_u64 v[222:223], s[26:27], 0, v[132:133]
	ds_read_b128 v[182:185], v160 offset:32768
	ds_read_b128 v[186:189], v160 offset:33792
	ds_read_b128 v[190:193], v160 offset:34816
	ds_read_b128 v[194:197], v160 offset:35840
	ds_read_b128 v[198:201], v160 offset:36864
	ds_read_b128 v[202:205], v160 offset:37888
	ds_read_b128 v[206:209], v160 offset:38912
	ds_read_b128 v[210:213], v160 offset:39936
	global_load_lds_dwordx4 v[222:223], off
	v_lshl_add_u64 v[222:223], s[26:27], 0, v[134:135]
	s_mov_b32 m0, s66
	s_nop 0
	global_load_lds_dwordx4 v[222:223], off
	s_waitcnt vmcnt(8)
	s_waitcnt lgkmcnt(0)
	s_barrier
	s_waitcnt lgkmcnt(0)
	v_mfma_f32_16x16x32_bf16 v[126:129], v[144:147], v[182:185], v[126:129]
	v_mfma_f32_16x16x32_bf16 v[122:125], v[152:155], v[182:185], v[122:125]
	v_mfma_f32_16x16x32_bf16 v[118:121], v[144:147], v[190:193], v[118:121]
	v_mfma_f32_16x16x32_bf16 v[114:117], v[152:155], v[190:193], v[114:117]
	v_mfma_f32_16x16x32_bf16 v[106:109], v[144:147], v[198:201], v[106:109]
	v_mfma_f32_16x16x32_bf16 v[98:101], v[152:155], v[198:201], v[98:101]
	v_mfma_f32_16x16x32_bf16 v[90:93], v[144:147], v[206:209], v[90:93]
	v_mfma_f32_16x16x32_bf16 v[82:85], v[152:155], v[206:209], v[82:85]
	v_mfma_f32_16x16x32_bf16 v[126:129], v[148:151], v[186:189], v[126:129]
	v_mfma_f32_16x16x32_bf16 v[122:125], v[162:165], v[186:189], v[122:125]
	v_mfma_f32_16x16x32_bf16 v[118:121], v[148:151], v[194:197], v[118:121]
	v_mfma_f32_16x16x32_bf16 v[114:117], v[162:165], v[194:197], v[114:117]
	v_mfma_f32_16x16x32_bf16 v[106:109], v[148:151], v[202:205], v[106:109]
	v_mfma_f32_16x16x32_bf16 v[98:101], v[162:165], v[202:205], v[98:101]
	v_mfma_f32_16x16x32_bf16 v[90:93], v[148:151], v[210:213], v[90:93]
	v_mfma_f32_16x16x32_bf16 v[82:85], v[162:165], v[210:213], v[82:85]
	v_mfma_f32_16x16x32_bf16 v[110:113], v[166:169], v[182:185], v[110:113]
	v_mfma_f32_16x16x32_bf16 v[102:105], v[174:177], v[182:185], v[102:105]
	v_mfma_f32_16x16x32_bf16 v[94:97], v[166:169], v[190:193], v[94:97]
	v_mfma_f32_16x16x32_bf16 v[86:89], v[174:177], v[190:193], v[86:89]
	v_mfma_f32_16x16x32_bf16 v[78:81], v[166:169], v[198:201], v[78:81]
	v_mfma_f32_16x16x32_bf16 v[74:77], v[174:177], v[198:201], v[74:77]
	v_mfma_f32_16x16x32_bf16 v[70:73], v[166:169], v[206:209], v[70:73]
	v_mfma_f32_16x16x32_bf16 v[66:69], v[174:177], v[206:209], v[66:69]
	v_mfma_f32_16x16x32_bf16 v[110:113], v[170:173], v[186:189], v[110:113]
	v_mfma_f32_16x16x32_bf16 v[102:105], v[178:181], v[186:189], v[102:105]
	v_mfma_f32_16x16x32_bf16 v[94:97], v[170:173], v[194:197], v[94:97]
	v_mfma_f32_16x16x32_bf16 v[86:89], v[178:181], v[194:197], v[86:89]
	v_mfma_f32_16x16x32_bf16 v[78:81], v[170:173], v[202:205], v[78:81]
	v_mfma_f32_16x16x32_bf16 v[74:77], v[178:181], v[202:205], v[74:77]
	v_mfma_f32_16x16x32_bf16 v[70:73], v[170:173], v[210:213], v[70:73]
	v_mfma_f32_16x16x32_bf16 v[66:69], v[178:181], v[210:213], v[66:69]
	s_barrier
	s_add_i32 s26, s81, s35
	v_lshl_add_u64 v[222:223], v[214:215], 0, s[14:15]
	s_mov_b32 m0, s26
	ds_read_b128 v[182:185], v160 offset:49152
	ds_read_b128 v[186:189], v160 offset:50176
	ds_read_b128 v[190:193], v160 offset:51200
	ds_read_b128 v[194:197], v160 offset:52224
	ds_read_b128 v[198:201], v160 offset:53248
	ds_read_b128 v[202:205], v160 offset:54272
	ds_read_b128 v[206:209], v160 offset:55296
	ds_read_b128 v[210:213], v160 offset:56320
	global_load_lds_dwordx4 v[222:223], off
	v_lshl_add_u64 v[222:223], v[214:215], 0, s[16:17]
	s_add_i32 m0, s26, 0x2000
	s_add_i32 s26, s82, s35
	global_load_lds_dwordx4 v[222:223], off
	v_lshl_add_u64 v[222:223], v[214:215], 0, s[20:21]
	s_mov_b32 m0, s26
	v_lshl_add_u64 v[214:215], v[214:215], 0, s[22:23]
	global_load_lds_dwordx4 v[222:223], off
	s_add_i32 m0, s26, 0x2000
	s_nop 0
	global_load_lds_dwordx4 v[214:215], off
	v_lshl_add_u64 v[214:215], v[216:217], 0, s[18:19]
	s_mov_b32 m0, s68
	s_nop 0
	global_load_lds_dwordx4 v[214:215], off
	v_lshl_add_u64 v[214:215], v[220:221], 0, s[18:19]
	s_mov_b32 m0, s69
	s_nop 0
	global_load_lds_dwordx4 v[214:215], off
	s_waitcnt vmcnt(8)
	s_waitcnt lgkmcnt(0)
	s_barrier
	s_waitcnt lgkmcnt(0)
	v_mfma_f32_16x16x32_bf16 v[62:65], v[144:147], v[182:185], v[62:65]
	v_mfma_f32_16x16x32_bf16 v[58:61], v[152:155], v[182:185], v[58:61]
	v_mfma_f32_16x16x32_bf16 v[54:57], v[144:147], v[190:193], v[54:57]
	v_mfma_f32_16x16x32_bf16 v[46:49], v[152:155], v[190:193], v[46:49]
	v_mfma_f32_16x16x32_bf16 v[38:41], v[144:147], v[198:201], v[38:41]
	v_mfma_f32_16x16x32_bf16 v[30:33], v[152:155], v[198:201], v[30:33]
	v_mfma_f32_16x16x32_bf16 v[22:25], v[144:147], v[206:209], v[22:25]
	v_mfma_f32_16x16x32_bf16 v[14:17], v[152:155], v[206:209], v[14:17]
	v_mfma_f32_16x16x32_bf16 v[62:65], v[148:151], v[186:189], v[62:65]
	v_mfma_f32_16x16x32_bf16 v[58:61], v[162:165], v[186:189], v[58:61]
	v_mfma_f32_16x16x32_bf16 v[54:57], v[148:151], v[194:197], v[54:57]
	v_mfma_f32_16x16x32_bf16 v[46:49], v[162:165], v[194:197], v[46:49]
	v_mfma_f32_16x16x32_bf16 v[38:41], v[148:151], v[202:205], v[38:41]
	v_mfma_f32_16x16x32_bf16 v[30:33], v[162:165], v[202:205], v[30:33]
	v_mfma_f32_16x16x32_bf16 v[22:25], v[148:151], v[210:213], v[22:25]
	v_mfma_f32_16x16x32_bf16 v[14:17], v[162:165], v[210:213], v[14:17]
	v_mfma_f32_16x16x32_bf16 v[50:53], v[166:169], v[182:185], v[50:53]
	v_mfma_f32_16x16x32_bf16 v[42:45], v[174:177], v[182:185], v[42:45]
	v_mfma_f32_16x16x32_bf16 v[34:37], v[166:169], v[190:193], v[34:37]
	v_mfma_f32_16x16x32_bf16 v[26:29], v[174:177], v[190:193], v[26:29]
	v_mfma_f32_16x16x32_bf16 v[18:21], v[166:169], v[198:201], v[18:21]
	v_mfma_f32_16x16x32_bf16 v[10:13], v[174:177], v[198:201], v[10:13]
	v_mfma_f32_16x16x32_bf16 v[6:9], v[166:169], v[206:209], v[6:9]
	v_mfma_f32_16x16x32_bf16 v[2:5], v[174:177], v[206:209], v[2:5]
	v_mfma_f32_16x16x32_bf16 v[50:53], v[170:173], v[186:189], v[50:53]
	v_mfma_f32_16x16x32_bf16 v[42:45], v[178:181], v[186:189], v[42:45]
	v_mfma_f32_16x16x32_bf16 v[34:37], v[170:173], v[194:197], v[34:37]
	v_mfma_f32_16x16x32_bf16 v[26:29], v[178:181], v[194:197], v[26:29]
	v_mfma_f32_16x16x32_bf16 v[18:21], v[170:173], v[202:205], v[18:21]
	v_mfma_f32_16x16x32_bf16 v[10:13], v[178:181], v[202:205], v[10:13]
	v_mfma_f32_16x16x32_bf16 v[6:9], v[170:173], v[210:213], v[6:9]
	v_mfma_f32_16x16x32_bf16 v[2:5], v[178:181], v[210:213], v[2:5]
	s_barrier
	s_add_i32 s80, s80, 2
	s_add_u32 s74, s74, 0x10000
	s_addc_u32 s75, s75, 0
	s_add_u32 s58, s58, 0x100
	s_addc_u32 s59, s59, 0
	s_cmp_gt_u32 s80, 29
	s_cbranch_scc0 .LBB0_1271
	s_and_b64 vcc, exec, s[24:25]
	s_cbranch_vccz .LBB0_1274
	s_barrier

.LBB0_1497:
	ds_read_b128 v[26:29], v186
	ds_read_b128 v[30:33], v186 offset:1024
	ds_read_b128 v[18:21], v186 offset:2048
	ds_read_b128 v[22:25], v186 offset:3072
	ds_read_b128 v[10:13], v187
	ds_read_b128 v[14:17], v187 offset:1024
	ds_read_b128 v[2:5], v187 offset:2048
	ds_read_b128 v[6:9], v187 offset:3072
	s_add_u32 s56, s4, 0xfffc0080
	s_addc_u32 s57, s5, -1
	s_cmp_eq_u32 s49, 12
	s_cselect_b64 vcc, -1, 0
	s_cselect_b32 s57, s2, s57
	s_cselect_b32 s56, s47, s56
	v_cndmask_b32_e32 v179, v177, v175, vcc
	v_cndmask_b32_e32 v178, v176, v174, vcc
	v_lshl_add_u64 v[180:181], s[4:5], 0, v[168:169]
	s_add_i32 m0, s62, 0xc000
	ds_read_b128 v[192:195], v188
	ds_read_b128 v[196:199], v188 offset:1024
	ds_read_b128 v[200:203], v188 offset:2048
	ds_read_b128 v[204:207], v188 offset:3072
	ds_read_b128 v[208:211], v188 offset:4096
	ds_read_b128 v[212:215], v188 offset:5120
	ds_read_b128 v[220:223], v188 offset:6144
	ds_read_b128 v[224:227], v188 offset:7168
	global_load_lds_dwordx4 v[180:181], off
	v_lshl_add_u64 v[180:181], s[4:5], 0, v[170:171]
	s_add_i32 m0, s62, 0xe000
	s_nop 0
	global_load_lds_dwordx4 v[180:181], off
	s_waitcnt vmcnt(8)
	s_waitcnt lgkmcnt(0)
	s_barrier
	s_waitcnt lgkmcnt(0)
	v_mfma_scale_f32_16x16x128_f8f6f4 v[158:161], v[26:33], v[192:199], v[158:161], v189, v190 op_sel_hi:[0,0,0]
	v_mfma_scale_f32_16x16x128_f8f6f4 v[150:153], v[18:25], v[192:199], v[150:153], v189, v190 op_sel_hi:[0,0,0]
	v_mfma_scale_f32_16x16x128_f8f6f4 v[142:145], v[26:33], v[200:207], v[142:145], v189, v190 op_sel_hi:[0,0,0]
	v_mfma_scale_f32_16x16x128_f8f6f4 v[134:137], v[18:25], v[200:207], v[134:137], v189, v190 op_sel_hi:[0,0,0]
	v_mfma_scale_f32_16x16x128_f8f6f4 v[126:129], v[26:33], v[208:215], v[126:129], v189, v190 op_sel_hi:[0,0,0]
	v_mfma_scale_f32_16x16x128_f8f6f4 v[118:121], v[18:25], v[208:215], v[118:121], v189, v190 op_sel_hi:[0,0,0]
	v_mfma_scale_f32_16x16x128_f8f6f4 v[110:113], v[26:33], v[220:227], v[110:113], v189, v190 op_sel_hi:[0,0,0]
	v_mfma_scale_f32_16x16x128_f8f6f4 v[102:105], v[18:25], v[220:227], v[102:105], v189, v190 op_sel_hi:[0,0,0]
	v_mfma_scale_f32_16x16x128_f8f6f4 v[154:157], v[10:17], v[192:199], v[154:157], v189, v190 op_sel_hi:[0,0,0]
	v_mfma_scale_f32_16x16x128_f8f6f4 v[146:149], v[2:9], v[192:199], v[146:149], v189, v190 op_sel_hi:[0,0,0]
	v_mfma_scale_f32_16x16x128_f8f6f4 v[138:141], v[10:17], v[200:207], v[138:141], v189, v190 op_sel_hi:[0,0,0]
	v_mfma_scale_f32_16x16x128_f8f6f4 v[130:133], v[2:9], v[200:207], v[130:133], v189, v190 op_sel_hi:[0,0,0]
	v_mfma_scale_f32_16x16x128_f8f6f4 v[122:125], v[10:17], v[208:215], v[122:125], v189, v190 op_sel_hi:[0,0,0]
	v_mfma_scale_f32_16x16x128_f8f6f4 v[114:117], v[2:9], v[208:215], v[114:117], v189, v190 op_sel_hi:[0,0,0]
	v_mfma_scale_f32_16x16x128_f8f6f4 v[106:109], v[10:17], v[220:227], v[106:109], v189, v190 op_sel_hi:[0,0,0]
	v_mfma_scale_f32_16x16x128_f8f6f4 v[98:101], v[2:9], v[220:227], v[98:101], v189, v190 op_sel_hi:[0,0,0]
	s_barrier
	s_add_i32 s73, s69, s61
	v_lshl_add_u64 v[178:179], v[178:179], 0, v[162:163]
	s_mov_b32 m0, s73
	ds_read_b128 v[192:195], v188 offset:16384
	ds_read_b128 v[196:199], v188 offset:17408
	ds_read_b128 v[200:203], v188 offset:18432
	ds_read_b128 v[204:207], v188 offset:19456
	ds_read_b128 v[208:211], v188 offset:20480
	ds_read_b128 v[212:215], v188 offset:21504
	ds_read_b128 v[220:223], v188 offset:22528
	ds_read_b128 v[224:227], v188 offset:23552
	global_load_lds_dwordx4 v[178:179], off
	v_lshl_add_u64 v[180:181], v[178:179], 0, s[10:11]
	s_add_i32 m0, s73, 0x2000
	s_add_i32 s73, s70, s61
	global_load_lds_dwordx4 v[180:181], off
	v_lshl_add_u64 v[180:181], v[178:179], 0, s[12:13]
	s_mov_b32 m0, s73
	v_lshl_add_u64 v[182:183], s[56:57], 0, v[166:167]
	global_load_lds_dwordx4 v[180:181], off
	v_lshl_add_u64 v[180:181], v[178:179], 0, s[14:15]
	s_add_i32 m0, s73, 0x2000
	s_nop 0
	global_load_lds_dwordx4 v[180:181], off
	v_lshl_add_u64 v[180:181], s[56:57], 0, v[164:165]
	s_mov_b32 m0, s62
	s_nop 0
	global_load_lds_dwordx4 v[180:181], off
	s_mov_b32 m0, s53
	s_nop 0
	global_load_lds_dwordx4 v[182:183], off
	s_waitcnt vmcnt(8)
	s_waitcnt lgkmcnt(0)
	s_barrier
	s_waitcnt lgkmcnt(0)
	v_mfma_scale_f32_16x16x128_f8f6f4 v[94:97], v[26:33], v[192:199], v[94:97], v189, v190 op_sel_hi:[0,0,0]
	v_mfma_scale_f32_16x16x128_f8f6f4 v[86:89], v[18:25], v[192:199], v[86:89], v189, v190 op_sel_hi:[0,0,0]
	v_mfma_scale_f32_16x16x128_f8f6f4 v[78:81], v[26:33], v[200:207], v[78:81], v189, v190 op_sel_hi:[0,0,0]
	v_mfma_scale_f32_16x16x128_f8f6f4 v[70:73], v[18:25], v[200:207], v[70:73], v189, v190 op_sel_hi:[0,0,0]
	v_mfma_scale_f32_16x16x128_f8f6f4 v[62:65], v[26:33], v[208:215], v[62:65], v189, v190 op_sel_hi:[0,0,0]
	v_mfma_scale_f32_16x16x128_f8f6f4 v[54:57], v[18:25], v[208:215], v[54:57], v189, v190 op_sel_hi:[0,0,0]
	v_mfma_scale_f32_16x16x128_f8f6f4 v[46:49], v[26:33], v[220:227], v[46:49], v189, v190 op_sel_hi:[0,0,0]
	v_mfma_scale_f32_16x16x128_f8f6f4 v[38:41], v[18:25], v[220:227], v[38:41], v189, v190 op_sel_hi:[0,0,0]
	v_mfma_scale_f32_16x16x128_f8f6f4 v[90:93], v[10:17], v[192:199], v[90:93], v189, v190 op_sel_hi:[0,0,0]
	v_mfma_scale_f32_16x16x128_f8f6f4 v[82:85], v[2:9], v[192:199], v[82:85], v189, v190 op_sel_hi:[0,0,0]
	v_mfma_scale_f32_16x16x128_f8f6f4 v[74:77], v[10:17], v[200:207], v[74:77], v189, v190 op_sel_hi:[0,0,0]
	v_mfma_scale_f32_16x16x128_f8f6f4 v[66:69], v[2:9], v[200:207], v[66:69], v189, v190 op_sel_hi:[0,0,0]
	v_mfma_scale_f32_16x16x128_f8f6f4 v[58:61], v[10:17], v[208:215], v[58:61], v189, v190 op_sel_hi:[0,0,0]
	v_mfma_scale_f32_16x16x128_f8f6f4 v[50:53], v[2:9], v[208:215], v[50:53], v189, v190 op_sel_hi:[0,0,0]
	v_mfma_scale_f32_16x16x128_f8f6f4 v[42:45], v[10:17], v[220:227], v[42:45], v189, v190 op_sel_hi:[0,0,0]
	v_mfma_scale_f32_16x16x128_f8f6f4 v[34:37], v[2:9], v[220:227], v[34:37], v189, v190 op_sel_hi:[0,0,0]
	s_barrier
	s_add_i32 s73, 0, 0x18000
	s_add_i32 s74, 0, 0x1c000
	v_add_u32_e32 v14, s73, v184
	v_add_u32_e32 v30, s74, v184
	ds_read_b128 v[2:5], v14
	ds_read_b128 v[6:9], v14 offset:1024
	ds_read_b128 v[10:13], v14 offset:2048
	ds_read_b128 v[14:17], v14 offset:3072
	ds_read_b128 v[18:21], v30
	ds_read_b128 v[22:25], v30 offset:1024
	ds_read_b128 v[26:29], v30 offset:2048
	ds_read_b128 v[30:33], v30 offset:3072
	s_add_u32 s56, s56, 0x40000
	s_addc_u32 s57, s57, 0
	s_mov_b32 m0, s63
	v_lshl_add_u64 v[216:217], s[56:57], 0, v[164:165]
	ds_read_b128 v[192:195], v188 offset:32768
	ds_read_b128 v[196:199], v188 offset:33792
	ds_read_b128 v[200:203], v188 offset:34816
	ds_read_b128 v[204:207], v188 offset:35840
	ds_read_b128 v[208:211], v188 offset:36864
	ds_read_b128 v[212:215], v188 offset:37888
	ds_read_b128 v[220:223], v188 offset:38912
	ds_read_b128 v[224:227], v188 offset:39936
	global_load_lds_dwordx4 v[216:217], off
	v_lshl_add_u64 v[216:217], s[56:57], 0, v[166:167]
	s_mov_b32 m0, s64
	s_nop 0
	global_load_lds_dwordx4 v[216:217], off
	s_waitcnt vmcnt(8)
	s_waitcnt lgkmcnt(0)
	s_barrier
	s_waitcnt lgkmcnt(0)
	v_mfma_scale_f32_16x16x128_f8f6f4 v[158:161], v[2:9], v[192:199], v[158:161], v189, v190 op_sel_hi:[0,0,0]
	v_mfma_scale_f32_16x16x128_f8f6f4 v[150:153], v[10:17], v[192:199], v[150:153], v189, v190 op_sel_hi:[0,0,0]
	v_mfma_scale_f32_16x16x128_f8f6f4 v[142:145], v[2:9], v[200:207], v[142:145], v189, v190 op_sel_hi:[0,0,0]
	v_mfma_scale_f32_16x16x128_f8f6f4 v[134:137], v[10:17], v[200:207], v[134:137], v189, v190 op_sel_hi:[0,0,0]
	v_mfma_scale_f32_16x16x128_f8f6f4 v[126:129], v[2:9], v[208:215], v[126:129], v189, v190 op_sel_hi:[0,0,0]
	v_mfma_scale_f32_16x16x128_f8f6f4 v[118:121], v[10:17], v[208:215], v[118:121], v189, v190 op_sel_hi:[0,0,0]
	v_mfma_scale_f32_16x16x128_f8f6f4 v[110:113], v[2:9], v[220:227], v[110:113], v189, v190 op_sel_hi:[0,0,0]
	v_mfma_scale_f32_16x16x128_f8f6f4 v[102:105], v[10:17], v[220:227], v[102:105], v189, v190 op_sel_hi:[0,0,0]
	v_mfma_scale_f32_16x16x128_f8f6f4 v[154:157], v[18:25], v[192:199], v[154:157], v189, v190 op_sel_hi:[0,0,0]
	v_mfma_scale_f32_16x16x128_f8f6f4 v[146:149], v[26:33], v[192:199], v[146:149], v189, v190 op_sel_hi:[0,0,0]
	v_mfma_scale_f32_16x16x128_f8f6f4 v[138:141], v[18:25], v[200:207], v[138:141], v189, v190 op_sel_hi:[0,0,0]
	v_mfma_scale_f32_16x16x128_f8f6f4 v[130:133], v[26:33], v[200:207], v[130:133], v189, v190 op_sel_hi:[0,0,0]
	v_mfma_scale_f32_16x16x128_f8f6f4 v[122:125], v[18:25], v[208:215], v[122:125], v189, v190 op_sel_hi:[0,0,0]
	v_mfma_scale_f32_16x16x128_f8f6f4 v[114:117], v[26:33], v[208:215], v[114:117], v189, v190 op_sel_hi:[0,0,0]
	v_mfma_scale_f32_16x16x128_f8f6f4 v[106:109], v[18:25], v[220:227], v[106:109], v189, v190 op_sel_hi:[0,0,0]
	v_mfma_scale_f32_16x16x128_f8f6f4 v[98:101], v[26:33], v[220:227], v[98:101], v189, v190 op_sel_hi:[0,0,0]
	s_barrier
	s_add_i32 s56, s73, s61
	v_lshl_add_u64 v[216:217], v[178:179], 0, s[20:21]
	s_mov_b32 m0, s56
	ds_read_b128 v[192:195], v188 offset:49152
	ds_read_b128 v[196:199], v188 offset:50176
	ds_read_b128 v[200:203], v188 offset:51200
	ds_read_b128 v[204:207], v188 offset:52224
	ds_read_b128 v[208:211], v188 offset:53248
	ds_read_b128 v[212:215], v188 offset:54272
	ds_read_b128 v[220:223], v188 offset:55296
	ds_read_b128 v[224:227], v188 offset:56320
	global_load_lds_dwordx4 v[216:217], off
	v_lshl_add_u64 v[216:217], v[178:179], 0, s[22:23]
	s_add_i32 m0, s56, 0x2000
	s_add_i32 s56, s74, s61
	global_load_lds_dwordx4 v[216:217], off
	v_lshl_add_u64 v[216:217], v[178:179], 0, s[26:27]
	s_mov_b32 m0, s56
	v_lshl_add_u64 v[178:179], v[178:179], 0, s[36:37]
	global_load_lds_dwordx4 v[216:217], off
	s_add_i32 m0, s56, 0x2000
	s_nop 0
	global_load_lds_dwordx4 v[178:179], off
	v_lshl_add_u64 v[178:179], v[180:181], 0, s[24:25]
	s_mov_b32 m0, s66
	s_nop 0
	global_load_lds_dwordx4 v[178:179], off
	v_lshl_add_u64 v[178:179], v[182:183], 0, s[24:25]
	s_mov_b32 m0, s67
	s_nop 0
	global_load_lds_dwordx4 v[178:179], off
	s_waitcnt vmcnt(8)
	s_waitcnt lgkmcnt(0)
	s_barrier
	s_waitcnt lgkmcnt(0)
	v_mfma_scale_f32_16x16x128_f8f6f4 v[94:97], v[2:9], v[192:199], v[94:97], v189, v190 op_sel_hi:[0,0,0]
	v_mfma_scale_f32_16x16x128_f8f6f4 v[86:89], v[10:17], v[192:199], v[86:89], v189, v190 op_sel_hi:[0,0,0]
	v_mfma_scale_f32_16x16x128_f8f6f4 v[78:81], v[2:9], v[200:207], v[78:81], v189, v190 op_sel_hi:[0,0,0]
	v_mfma_scale_f32_16x16x128_f8f6f4 v[70:73], v[10:17], v[200:207], v[70:73], v189, v190 op_sel_hi:[0,0,0]
	v_mfma_scale_f32_16x16x128_f8f6f4 v[62:65], v[2:9], v[208:215], v[62:65], v189, v190 op_sel_hi:[0,0,0]
	v_mfma_scale_f32_16x16x128_f8f6f4 v[54:57], v[10:17], v[208:215], v[54:57], v189, v190 op_sel_hi:[0,0,0]
	v_mfma_scale_f32_16x16x128_f8f6f4 v[46:49], v[2:9], v[220:227], v[46:49], v189, v190 op_sel_hi:[0,0,0]
	v_mfma_scale_f32_16x16x128_f8f6f4 v[38:41], v[10:17], v[220:227], v[38:41], v189, v190 op_sel_hi:[0,0,0]
	v_mfma_scale_f32_16x16x128_f8f6f4 v[90:93], v[18:25], v[192:199], v[90:93], v189, v190 op_sel_hi:[0,0,0]
	v_mfma_scale_f32_16x16x128_f8f6f4 v[82:85], v[26:33], v[192:199], v[82:85], v189, v190 op_sel_hi:[0,0,0]
	v_mfma_scale_f32_16x16x128_f8f6f4 v[74:77], v[18:25], v[200:207], v[74:77], v189, v190 op_sel_hi:[0,0,0]
	v_mfma_scale_f32_16x16x128_f8f6f4 v[66:69], v[26:33], v[200:207], v[66:69], v189, v190 op_sel_hi:[0,0,0]
	v_mfma_scale_f32_16x16x128_f8f6f4 v[58:61], v[18:25], v[208:215], v[58:61], v189, v190 op_sel_hi:[0,0,0]
	v_mfma_scale_f32_16x16x128_f8f6f4 v[50:53], v[26:33], v[208:215], v[50:53], v189, v190 op_sel_hi:[0,0,0]
	v_mfma_scale_f32_16x16x128_f8f6f4 v[42:45], v[18:25], v[220:227], v[42:45], v189, v190 op_sel_hi:[0,0,0]
	v_mfma_scale_f32_16x16x128_f8f6f4 v[34:37], v[26:33], v[220:227], v[34:37], v189, v190 op_sel_hi:[0,0,0]
	s_barrier
	s_add_i32 s49, s49, 2
	s_add_u32 s4, s4, 0x100
	s_addc_u32 s5, s5, 0
	s_cmp_gt_u32 s49, 13
	v_lshl_add_u64 v[176:177], v[176:177], 0, s[40:41]
	s_cbranch_scc0 .LBB0_1497
	s_and_b64 vcc, exec, s[38:39]
	s_cbranch_vccz .LBB0_1500
	s_barrier

.LBB0_1568:
	ds_read_b128 v[26:29], v186
	ds_read_b128 v[30:33], v186 offset:1024
	ds_read_b128 v[18:21], v186 offset:2048
	ds_read_b128 v[22:25], v186 offset:3072
	ds_read_b128 v[10:13], v187
	ds_read_b128 v[14:17], v187 offset:1024
	ds_read_b128 v[2:5], v187 offset:2048
	ds_read_b128 v[6:9], v187 offset:3072
	s_add_u32 s58, s56, 0xfff50080
	s_addc_u32 s59, s57, -1
	s_cmp_eq_u32 s53, 40
	s_cselect_b64 vcc, -1, 0
	s_cselect_b32 s59, s5, s59
	s_cselect_b32 s58, s4, s58
	v_cndmask_b32_e32 v179, v177, v175, vcc
	v_cndmask_b32_e32 v178, v176, v174, vcc
	v_lshl_add_u64 v[180:181], s[56:57], 0, v[170:171]
	s_add_i32 m0, s61, 0xc000
	ds_read_b128 v[192:195], v188
	ds_read_b128 v[196:199], v188 offset:1024
	ds_read_b128 v[200:203], v188 offset:2048
	ds_read_b128 v[204:207], v188 offset:3072
	ds_read_b128 v[208:211], v188 offset:4096
	ds_read_b128 v[212:215], v188 offset:5120
	ds_read_b128 v[220:223], v188 offset:6144
	ds_read_b128 v[224:227], v188 offset:7168
	global_load_lds_dwordx4 v[180:181], off
	v_lshl_add_u64 v[180:181], s[56:57], 0, v[172:173]
	s_add_i32 m0, s61, 0xe000
	s_nop 0
	global_load_lds_dwordx4 v[180:181], off
	s_waitcnt vmcnt(8)
	s_waitcnt lgkmcnt(0)
	s_barrier
	s_waitcnt lgkmcnt(0)
	v_mfma_scale_f32_16x16x128_f8f6f4 v[158:161], v[26:33], v[192:199], v[158:161], v189, v190 op_sel_hi:[0,0,0]
	v_mfma_scale_f32_16x16x128_f8f6f4 v[154:157], v[18:25], v[192:199], v[154:157], v189, v190 op_sel_hi:[0,0,0]
	v_mfma_scale_f32_16x16x128_f8f6f4 v[150:153], v[26:33], v[200:207], v[150:153], v189, v190 op_sel_hi:[0,0,0]
	v_mfma_scale_f32_16x16x128_f8f6f4 v[142:145], v[18:25], v[200:207], v[142:145], v189, v190 op_sel_hi:[0,0,0]
	v_mfma_scale_f32_16x16x128_f8f6f4 v[134:137], v[26:33], v[208:215], v[134:137], v189, v190 op_sel_hi:[0,0,0]
	v_mfma_scale_f32_16x16x128_f8f6f4 v[126:129], v[18:25], v[208:215], v[126:129], v189, v190 op_sel_hi:[0,0,0]
	v_mfma_scale_f32_16x16x128_f8f6f4 v[118:121], v[26:33], v[220:227], v[118:121], v189, v190 op_sel_hi:[0,0,0]
	v_mfma_scale_f32_16x16x128_f8f6f4 v[110:113], v[18:25], v[220:227], v[110:113], v189, v190 op_sel_hi:[0,0,0]
	v_mfma_scale_f32_16x16x128_f8f6f4 v[146:149], v[10:17], v[192:199], v[146:149], v189, v190 op_sel_hi:[0,0,0]
	v_mfma_scale_f32_16x16x128_f8f6f4 v[138:141], v[2:9], v[192:199], v[138:141], v189, v190 op_sel_hi:[0,0,0]
	v_mfma_scale_f32_16x16x128_f8f6f4 v[130:133], v[10:17], v[200:207], v[130:133], v189, v190 op_sel_hi:[0,0,0]
	v_mfma_scale_f32_16x16x128_f8f6f4 v[122:125], v[2:9], v[200:207], v[122:125], v189, v190 op_sel_hi:[0,0,0]
	v_mfma_scale_f32_16x16x128_f8f6f4 v[114:117], v[10:17], v[208:215], v[114:117], v189, v190 op_sel_hi:[0,0,0]
	v_mfma_scale_f32_16x16x128_f8f6f4 v[106:109], v[2:9], v[208:215], v[106:109], v189, v190 op_sel_hi:[0,0,0]
	v_mfma_scale_f32_16x16x128_f8f6f4 v[102:105], v[10:17], v[220:227], v[102:105], v189, v190 op_sel_hi:[0,0,0]
	v_mfma_scale_f32_16x16x128_f8f6f4 v[98:101], v[2:9], v[220:227], v[98:101], v189, v190 op_sel_hi:[0,0,0]
	s_barrier
	s_add_i32 s80, s69, s33
	v_lshl_add_u64 v[178:179], v[178:179], 0, v[164:165]
	s_mov_b32 m0, s80
	ds_read_b128 v[192:195], v188 offset:16384
	ds_read_b128 v[196:199], v188 offset:17408
	ds_read_b128 v[200:203], v188 offset:18432
	ds_read_b128 v[204:207], v188 offset:19456
	ds_read_b128 v[208:211], v188 offset:20480
	ds_read_b128 v[212:215], v188 offset:21504
	ds_read_b128 v[220:223], v188 offset:22528
	ds_read_b128 v[224:227], v188 offset:23552
	global_load_lds_dwordx4 v[178:179], off
	v_lshl_add_u64 v[180:181], v[178:179], 0, s[10:11]
	s_add_i32 m0, s80, 0x2000
	s_add_i32 s80, s70, s33
	global_load_lds_dwordx4 v[180:181], off
	v_lshl_add_u64 v[180:181], v[178:179], 0, s[12:13]
	s_mov_b32 m0, s80
	v_lshl_add_u64 v[182:183], s[58:59], 0, v[168:169]
	global_load_lds_dwordx4 v[180:181], off
	v_lshl_add_u64 v[180:181], v[178:179], 0, s[14:15]
	s_add_i32 m0, s80, 0x2000
	s_nop 0
	global_load_lds_dwordx4 v[180:181], off
	v_lshl_add_u64 v[180:181], s[58:59], 0, v[166:167]
	s_mov_b32 m0, s61
	s_nop 0
	global_load_lds_dwordx4 v[180:181], off
	s_mov_b32 m0, s62
	s_nop 0
	global_load_lds_dwordx4 v[182:183], off
	s_waitcnt vmcnt(8)
	s_waitcnt lgkmcnt(0)
	s_barrier
	s_waitcnt lgkmcnt(0)
	v_mfma_scale_f32_16x16x128_f8f6f4 v[94:97], v[26:33], v[192:199], v[94:97], v189, v190 op_sel_hi:[0,0,0]
	v_mfma_scale_f32_16x16x128_f8f6f4 v[90:93], v[18:25], v[192:199], v[90:93], v189, v190 op_sel_hi:[0,0,0]
	v_mfma_scale_f32_16x16x128_f8f6f4 v[86:89], v[26:33], v[200:207], v[86:89], v189, v190 op_sel_hi:[0,0,0]
	v_mfma_scale_f32_16x16x128_f8f6f4 v[78:81], v[18:25], v[200:207], v[78:81], v189, v190 op_sel_hi:[0,0,0]
	v_mfma_scale_f32_16x16x128_f8f6f4 v[70:73], v[26:33], v[208:215], v[70:73], v189, v190 op_sel_hi:[0,0,0]
	v_mfma_scale_f32_16x16x128_f8f6f4 v[62:65], v[18:25], v[208:215], v[62:65], v189, v190 op_sel_hi:[0,0,0]
	v_mfma_scale_f32_16x16x128_f8f6f4 v[54:57], v[26:33], v[220:227], v[54:57], v189, v190 op_sel_hi:[0,0,0]
	v_mfma_scale_f32_16x16x128_f8f6f4 v[46:49], v[18:25], v[220:227], v[46:49], v189, v190 op_sel_hi:[0,0,0]
	v_mfma_scale_f32_16x16x128_f8f6f4 v[82:85], v[10:17], v[192:199], v[82:85], v189, v190 op_sel_hi:[0,0,0]
	v_mfma_scale_f32_16x16x128_f8f6f4 v[74:77], v[2:9], v[192:199], v[74:77], v189, v190 op_sel_hi:[0,0,0]
	v_mfma_scale_f32_16x16x128_f8f6f4 v[66:69], v[10:17], v[200:207], v[66:69], v189, v190 op_sel_hi:[0,0,0]
	v_mfma_scale_f32_16x16x128_f8f6f4 v[58:61], v[2:9], v[200:207], v[58:61], v189, v190 op_sel_hi:[0,0,0]
	v_mfma_scale_f32_16x16x128_f8f6f4 v[50:53], v[10:17], v[208:215], v[50:53], v189, v190 op_sel_hi:[0,0,0]
	v_mfma_scale_f32_16x16x128_f8f6f4 v[42:45], v[2:9], v[208:215], v[42:45], v189, v190 op_sel_hi:[0,0,0]
	v_mfma_scale_f32_16x16x128_f8f6f4 v[38:41], v[10:17], v[220:227], v[38:41], v189, v190 op_sel_hi:[0,0,0]
	v_mfma_scale_f32_16x16x128_f8f6f4 v[34:37], v[2:9], v[220:227], v[34:37], v189, v190 op_sel_hi:[0,0,0]
	s_barrier
	s_add_i32 s80, 0, 0x18000
	s_add_i32 s81, 0, 0x1c000
	v_add_u32_e32 v14, s80, v184
	v_add_u32_e32 v30, s81, v184
	ds_read_b128 v[2:5], v14
	ds_read_b128 v[6:9], v14 offset:1024
	ds_read_b128 v[10:13], v14 offset:2048
	ds_read_b128 v[14:17], v14 offset:3072
	ds_read_b128 v[18:21], v30
	ds_read_b128 v[22:25], v30 offset:1024
	ds_read_b128 v[26:29], v30 offset:2048
	ds_read_b128 v[30:33], v30 offset:3072
	s_add_u32 s58, s58, 0xb0000
	s_addc_u32 s59, s59, 0
	s_mov_b32 m0, s63
	v_lshl_add_u64 v[216:217], s[58:59], 0, v[166:167]
	ds_read_b128 v[192:195], v188 offset:32768
	ds_read_b128 v[196:199], v188 offset:33792
	ds_read_b128 v[200:203], v188 offset:34816
	ds_read_b128 v[204:207], v188 offset:35840
	ds_read_b128 v[208:211], v188 offset:36864
	ds_read_b128 v[212:215], v188 offset:37888
	ds_read_b128 v[220:223], v188 offset:38912
	ds_read_b128 v[224:227], v188 offset:39936
	global_load_lds_dwordx4 v[216:217], off
	v_lshl_add_u64 v[216:217], s[58:59], 0, v[168:169]
	s_mov_b32 m0, s64
	s_nop 0
	global_load_lds_dwordx4 v[216:217], off
	s_waitcnt vmcnt(8)
	s_waitcnt lgkmcnt(0)
	s_barrier
	s_waitcnt lgkmcnt(0)
	v_mfma_scale_f32_16x16x128_f8f6f4 v[158:161], v[2:9], v[192:199], v[158:161], v189, v190 op_sel_hi:[0,0,0]
	v_mfma_scale_f32_16x16x128_f8f6f4 v[154:157], v[10:17], v[192:199], v[154:157], v189, v190 op_sel_hi:[0,0,0]
	v_mfma_scale_f32_16x16x128_f8f6f4 v[150:153], v[2:9], v[200:207], v[150:153], v189, v190 op_sel_hi:[0,0,0]
	v_mfma_scale_f32_16x16x128_f8f6f4 v[142:145], v[10:17], v[200:207], v[142:145], v189, v190 op_sel_hi:[0,0,0]
	v_mfma_scale_f32_16x16x128_f8f6f4 v[134:137], v[2:9], v[208:215], v[134:137], v189, v190 op_sel_hi:[0,0,0]
	v_mfma_scale_f32_16x16x128_f8f6f4 v[126:129], v[10:17], v[208:215], v[126:129], v189, v190 op_sel_hi:[0,0,0]
	v_mfma_scale_f32_16x16x128_f8f6f4 v[118:121], v[2:9], v[220:227], v[118:121], v189, v190 op_sel_hi:[0,0,0]
	v_mfma_scale_f32_16x16x128_f8f6f4 v[110:113], v[10:17], v[220:227], v[110:113], v189, v190 op_sel_hi:[0,0,0]
	v_mfma_scale_f32_16x16x128_f8f6f4 v[146:149], v[18:25], v[192:199], v[146:149], v189, v190 op_sel_hi:[0,0,0]
	v_mfma_scale_f32_16x16x128_f8f6f4 v[138:141], v[26:33], v[192:199], v[138:141], v189, v190 op_sel_hi:[0,0,0]
	v_mfma_scale_f32_16x16x128_f8f6f4 v[130:133], v[18:25], v[200:207], v[130:133], v189, v190 op_sel_hi:[0,0,0]
	v_mfma_scale_f32_16x16x128_f8f6f4 v[122:125], v[26:33], v[200:207], v[122:125], v189, v190 op_sel_hi:[0,0,0]
	v_mfma_scale_f32_16x16x128_f8f6f4 v[114:117], v[18:25], v[208:215], v[114:117], v189, v190 op_sel_hi:[0,0,0]
	v_mfma_scale_f32_16x16x128_f8f6f4 v[106:109], v[26:33], v[208:215], v[106:109], v189, v190 op_sel_hi:[0,0,0]
	v_mfma_scale_f32_16x16x128_f8f6f4 v[102:105], v[18:25], v[220:227], v[102:105], v189, v190 op_sel_hi:[0,0,0]
	v_mfma_scale_f32_16x16x128_f8f6f4 v[98:101], v[26:33], v[220:227], v[98:101], v189, v190 op_sel_hi:[0,0,0]
	s_barrier
	s_add_i32 s58, s80, s33
	v_lshl_add_u64 v[216:217], v[178:179], 0, s[24:25]
	s_mov_b32 m0, s58
	ds_read_b128 v[192:195], v188 offset:49152
	ds_read_b128 v[196:199], v188 offset:50176
	ds_read_b128 v[200:203], v188 offset:51200
	ds_read_b128 v[204:207], v188 offset:52224
	ds_read_b128 v[208:211], v188 offset:53248
	ds_read_b128 v[212:215], v188 offset:54272
	ds_read_b128 v[220:223], v188 offset:55296
	ds_read_b128 v[224:227], v188 offset:56320
	global_load_lds_dwordx4 v[216:217], off
	v_lshl_add_u64 v[216:217], v[178:179], 0, s[26:27]
	s_add_i32 m0, s58, 0x2000
	s_add_i32 s58, s81, s33
	global_load_lds_dwordx4 v[216:217], off
	v_lshl_add_u64 v[216:217], v[178:179], 0, s[38:39]
	s_mov_b32 m0, s58
	v_lshl_add_u64 v[178:179], v[178:179], 0, s[40:41]
	global_load_lds_dwordx4 v[216:217], off
	s_add_i32 m0, s58, 0x2000
	s_nop 0
	global_load_lds_dwordx4 v[178:179], off
	v_lshl_add_u64 v[178:179], v[180:181], 0, s[36:37]
	s_mov_b32 m0, s66
	s_nop 0
	global_load_lds_dwordx4 v[178:179], off
	v_lshl_add_u64 v[178:179], v[182:183], 0, s[36:37]
	s_mov_b32 m0, s67
	s_nop 0
	global_load_lds_dwordx4 v[178:179], off
	s_waitcnt vmcnt(8)
	s_waitcnt lgkmcnt(0)
	s_barrier
	s_waitcnt lgkmcnt(0)
	v_mfma_scale_f32_16x16x128_f8f6f4 v[94:97], v[2:9], v[192:199], v[94:97], v189, v190 op_sel_hi:[0,0,0]
	v_mfma_scale_f32_16x16x128_f8f6f4 v[90:93], v[10:17], v[192:199], v[90:93], v189, v190 op_sel_hi:[0,0,0]
	v_mfma_scale_f32_16x16x128_f8f6f4 v[86:89], v[2:9], v[200:207], v[86:89], v189, v190 op_sel_hi:[0,0,0]
	v_mfma_scale_f32_16x16x128_f8f6f4 v[78:81], v[10:17], v[200:207], v[78:81], v189, v190 op_sel_hi:[0,0,0]
	v_mfma_scale_f32_16x16x128_f8f6f4 v[70:73], v[2:9], v[208:215], v[70:73], v189, v190 op_sel_hi:[0,0,0]
	v_mfma_scale_f32_16x16x128_f8f6f4 v[62:65], v[10:17], v[208:215], v[62:65], v189, v190 op_sel_hi:[0,0,0]
	v_mfma_scale_f32_16x16x128_f8f6f4 v[54:57], v[2:9], v[220:227], v[54:57], v189, v190 op_sel_hi:[0,0,0]
	v_mfma_scale_f32_16x16x128_f8f6f4 v[46:49], v[10:17], v[220:227], v[46:49], v189, v190 op_sel_hi:[0,0,0]
	v_mfma_scale_f32_16x16x128_f8f6f4 v[82:85], v[18:25], v[192:199], v[82:85], v189, v190 op_sel_hi:[0,0,0]
	v_mfma_scale_f32_16x16x128_f8f6f4 v[74:77], v[26:33], v[192:199], v[74:77], v189, v190 op_sel_hi:[0,0,0]
	v_mfma_scale_f32_16x16x128_f8f6f4 v[66:69], v[18:25], v[200:207], v[66:69], v189, v190 op_sel_hi:[0,0,0]
	v_mfma_scale_f32_16x16x128_f8f6f4 v[58:61], v[26:33], v[200:207], v[58:61], v189, v190 op_sel_hi:[0,0,0]
	v_mfma_scale_f32_16x16x128_f8f6f4 v[50:53], v[18:25], v[208:215], v[50:53], v189, v190 op_sel_hi:[0,0,0]
	v_mfma_scale_f32_16x16x128_f8f6f4 v[42:45], v[26:33], v[208:215], v[42:45], v189, v190 op_sel_hi:[0,0,0]
	v_mfma_scale_f32_16x16x128_f8f6f4 v[38:41], v[18:25], v[220:227], v[38:41], v189, v190 op_sel_hi:[0,0,0]
	v_mfma_scale_f32_16x16x128_f8f6f4 v[34:37], v[26:33], v[220:227], v[34:37], v189, v190 op_sel_hi:[0,0,0]
	s_barrier
	s_add_i32 s53, s53, 2
	s_add_u32 s56, s56, 0x100
	s_addc_u32 s57, s57, 0
	s_cmp_gt_u32 s53, 41
	v_lshl_add_u64 v[176:177], v[176:177], 0, s[44:45]
	s_cbranch_scc0 .LBB0_1568
	s_and_b64 vcc, exec, s[42:43]
	s_cbranch_vccz .LBB0_1571
	s_barrier
